# c7
# speedup vs baseline: 1.0298x; 1.0003x over previous
.LBB2_3:
	s_add_i32 s44, s62, 0xfffff000
	s_and_b32 s44, s44, 0x1000
	ds_read_b128 v[202:205], v175
	ds_read_b128 v[206:209], v175 offset:256
	ds_read_b128 v[210:213], v175 offset:512
	ds_read_b128 v[214:217], v175 offset:768
	ds_read_b128 v[218:221], v175 offset:1024
	ds_read_b128 v[222:225], v175 offset:1280
	ds_read_b128 v[226:229], v175 offset:1536
	ds_read_b128 v[230:233], v175 offset:1792
	ds_read2_b64 v[178:181], v171 offset1:1
	ds_read2_b64 v[182:185], v171 offset0:2 offset1:48
	ds_read2_b64 v[186:189], v171 offset0:49 offset1:50
	s_mov_b32 m0, s59
	ds_read2_b64 v[190:193], v171 offset0:96 offset1:97
	global_load_lds_dwordx4 v144, s[76:77]
	s_mov_b32 m0, s58
	ds_read2_b64 v[194:197], v171 offset0:98 offset1:144
	global_load_lds_dwordx4 v145, s[76:77]
	s_mov_b32 m0, s57
	ds_read2_b64 v[198:201], v171 offset0:145 offset1:146
	global_load_lds_dwordx4 v146, s[76:77]
	v_add_u32_e32 v152, s44, v176
	ds_read_u16 v240, v152
	ds_read_u16 v241, v152 offset:32
	ds_read_u16 v242, v152 offset:64
	s_add_i32 s44, s62, 0xfffff800
	s_and_b32 s44, s44, 0x1800
	s_add_i32 m0, s50, s44
	ds_read_u16 v243, v152 offset:96
	global_load_lds_dword v150, s[80:81]
	s_waitcnt vmcnt(6)
	s_waitcnt lgkmcnt(0)
	s_barrier
	v_mfma_scale_f32_16x16x128_f8f6f4 v[126:129], v[202:205], v[178:183], v[126:129], v177, v240 op_sel_hi:[0,0,0] cbsz:4 blgp:2
	v_mfma_scale_f32_16x16x128_f8f6f4 v[122:125], v[206:209], v[178:183], v[122:125], v177, v240 op_sel_hi:[0,0,0] cbsz:4 blgp:2
	v_mfma_scale_f32_16x16x128_f8f6f4 v[114:117], v[210:213], v[178:183], v[114:117], v177, v240 op_sel_hi:[0,0,0] cbsz:4 blgp:2
	v_mfma_scale_f32_16x16x128_f8f6f4 v[102:105], v[214:217], v[178:183], v[102:105], v177, v240 op_sel_hi:[0,0,0] cbsz:4 blgp:2
	v_mfma_scale_f32_16x16x128_f8f6f4 v[86:89], v[218:221], v[178:183], v[86:89], v177, v240 op_sel_hi:[0,0,0] cbsz:4 blgp:2
	v_mfma_scale_f32_16x16x128_f8f6f4 v[70:73], v[222:225], v[178:183], v[70:73], v177, v240 op_sel_hi:[0,0,0] cbsz:4 blgp:2
	v_mfma_scale_f32_16x16x128_f8f6f4 v[54:57], v[226:229], v[178:183], v[54:57], v177, v240 op_sel_hi:[0,0,0] cbsz:4 blgp:2
	v_mfma_scale_f32_16x16x128_f8f6f4 v[38:41], v[230:233], v[178:183], v[38:41], v177, v240 op_sel_hi:[0,0,0] cbsz:4 blgp:2
	v_mfma_scale_f32_16x16x128_f8f6f4 v[118:121], v[202:205], v[184:189], v[118:121], v177, v241 op_sel_hi:[0,0,0] cbsz:4 blgp:2
	v_mfma_scale_f32_16x16x128_f8f6f4 v[110:113], v[206:209], v[184:189], v[110:113], v177, v241 op_sel_hi:[0,0,0] cbsz:4 blgp:2
	v_mfma_scale_f32_16x16x128_f8f6f4 v[98:101], v[210:213], v[184:189], v[98:101], v177, v241 op_sel_hi:[0,0,0] cbsz:4 blgp:2
	v_mfma_scale_f32_16x16x128_f8f6f4 v[82:85], v[214:217], v[184:189], v[82:85], v177, v241 op_sel_hi:[0,0,0] cbsz:4 blgp:2
	v_mfma_scale_f32_16x16x128_f8f6f4 v[66:69], v[218:221], v[184:189], v[66:69], v177, v241 op_sel_hi:[0,0,0] cbsz:4 blgp:2
	v_mfma_scale_f32_16x16x128_f8f6f4 v[50:53], v[222:225], v[184:189], v[50:53], v177, v241 op_sel_hi:[0,0,0] cbsz:4 blgp:2
	v_mfma_scale_f32_16x16x128_f8f6f4 v[34:37], v[226:229], v[184:189], v[34:37], v177, v241 op_sel_hi:[0,0,0] cbsz:4 blgp:2
	v_mfma_scale_f32_16x16x128_f8f6f4 v[106:109], v[202:205], v[190:195], v[106:109], v177, v242 op_sel_hi:[0,0,0] cbsz:4 blgp:2
	v_mfma_scale_f32_16x16x128_f8f6f4 v[94:97], v[206:209], v[190:195], v[94:97], v177, v242 op_sel_hi:[0,0,0] cbsz:4 blgp:2
	v_mfma_scale_f32_16x16x128_f8f6f4 v[78:81], v[210:213], v[190:195], v[78:81], v177, v242 op_sel_hi:[0,0,0] cbsz:4 blgp:2
	v_mfma_scale_f32_16x16x128_f8f6f4 v[62:65], v[214:217], v[190:195], v[62:65], v177, v242 op_sel_hi:[0,0,0] cbsz:4 blgp:2
	v_mfma_scale_f32_16x16x128_f8f6f4 v[46:49], v[218:221], v[190:195], v[46:49], v177, v242 op_sel_hi:[0,0,0] cbsz:4 blgp:2
	v_mfma_scale_f32_16x16x128_f8f6f4 v[30:33], v[222:225], v[190:195], v[30:33], v177, v242 op_sel_hi:[0,0,0] cbsz:4 blgp:2
	v_mfma_scale_f32_16x16x128_f8f6f4 v[90:93], v[202:205], v[196:201], v[90:93], v177, v243 op_sel_hi:[0,0,0] cbsz:4 blgp:2
	v_mfma_scale_f32_16x16x128_f8f6f4 v[74:77], v[206:209], v[196:201], v[74:77], v177, v243 op_sel_hi:[0,0,0] cbsz:4 blgp:2
	v_mfma_scale_f32_16x16x128_f8f6f4 v[58:61], v[210:213], v[196:201], v[58:61], v177, v243 op_sel_hi:[0,0,0] cbsz:4 blgp:2
	v_mfma_scale_f32_16x16x128_f8f6f4 v[42:45], v[214:217], v[196:201], v[42:45], v177, v243 op_sel_hi:[0,0,0] cbsz:4 blgp:2
	v_mfma_scale_f32_16x16x128_f8f6f4 v[26:29], v[218:221], v[196:201], v[26:29], v177, v243 op_sel_hi:[0,0,0] cbsz:4 blgp:2
	v_mfma_scale_f32_16x16x128_f8f6f4 v[178:181], v[230:233], v[184:189], v[22:25], v177, v241 op_sel_hi:[0,0,0] cbsz:4 blgp:2
	v_mfma_scale_f32_16x16x128_f8f6f4 v[182:185], v[226:229], v[190:195], v[18:21], v177, v242 op_sel_hi:[0,0,0] cbsz:4 blgp:2
	v_mfma_scale_f32_16x16x128_f8f6f4 v[186:189], v[230:233], v[190:195], v[10:13], v177, v242 op_sel_hi:[0,0,0] cbsz:4 blgp:2
	v_mfma_scale_f32_16x16x128_f8f6f4 v[190:193], v[222:225], v[196:201], v[14:17], v177, v243 op_sel_hi:[0,0,0] cbsz:4 blgp:2
	v_mfma_scale_f32_16x16x128_f8f6f4 v[234:237], v[226:229], v[196:201], v[6:9], v177, v243 op_sel_hi:[0,0,0] cbsz:4 blgp:2
	v_mfma_scale_f32_16x16x128_f8f6f4 v[194:197], v[230:233], v[196:201], v[2:5], v177, v243 op_sel_hi:[0,0,0] cbsz:4 blgp:2
	s_barrier
	ds_read2_b64 v[2:5], v167 offset1:1
	s_mov_b32 m0, s54
	ds_read2_b64 v[6:9], v167 offset0:2 offset1:48
	global_load_lds_dwordx4 v147, s[76:77]
	s_mov_b32 m0, s52
	ds_read2_b64 v[10:13], v167 offset0:49 offset1:50
	global_load_lds_dwordx4 v148, s[76:77]
	s_mov_b32 m0, s51
	ds_read2_b64 v[14:17], v167 offset0:96 offset1:97
	global_load_lds_dwordx4 v149, s[76:77]
	s_mov_b32 m0, s15
	ds_read2_b64 v[18:21], v167 offset0:98 offset1:144
	global_load_lds_dwordx4 v142, s[72:73]
	s_mov_b32 m0, s46
	ds_read2_b64 v[22:25], v167 offset0:145 offset1:146
	global_load_lds_dwordx4 v143, s[72:73]
	s_waitcnt vmcnt(5)
	s_waitcnt lgkmcnt(0)
	s_barrier
	v_mfma_scale_f32_16x16x128_f8f6f4 v[126:129], v[202:205], v[2:7], v[126:129], v177, v240 op_sel:[0,1,0] op_sel_hi:[0,0,0] cbsz:4 blgp:2
	v_mfma_scale_f32_16x16x128_f8f6f4 v[122:125], v[206:209], v[2:7], v[122:125], v177, v240 op_sel:[0,1,0] op_sel_hi:[0,0,0] cbsz:4 blgp:2
	v_mfma_scale_f32_16x16x128_f8f6f4 v[114:117], v[210:213], v[2:7], v[114:117], v177, v240 op_sel:[0,1,0] op_sel_hi:[0,0,0] cbsz:4 blgp:2
	v_mfma_scale_f32_16x16x128_f8f6f4 v[102:105], v[214:217], v[2:7], v[102:105], v177, v240 op_sel:[0,1,0] op_sel_hi:[0,0,0] cbsz:4 blgp:2
	v_mfma_scale_f32_16x16x128_f8f6f4 v[86:89], v[218:221], v[2:7], v[86:89], v177, v240 op_sel:[0,1,0] op_sel_hi:[0,0,0] cbsz:4 blgp:2
	v_mfma_scale_f32_16x16x128_f8f6f4 v[70:73], v[222:225], v[2:7], v[70:73], v177, v240 op_sel:[0,1,0] op_sel_hi:[0,0,0] cbsz:4 blgp:2
	v_mfma_scale_f32_16x16x128_f8f6f4 v[54:57], v[226:229], v[2:7], v[54:57], v177, v240 op_sel:[0,1,0] op_sel_hi:[0,0,0] cbsz:4 blgp:2
	v_mfma_scale_f32_16x16x128_f8f6f4 v[38:41], v[230:233], v[2:7], v[38:41], v177, v240 op_sel:[0,1,0] op_sel_hi:[0,0,0] cbsz:4 blgp:2
	v_mfma_scale_f32_16x16x128_f8f6f4 v[118:121], v[202:205], v[8:13], v[118:121], v177, v241 op_sel:[0,1,0] op_sel_hi:[0,0,0] cbsz:4 blgp:2
	v_mfma_scale_f32_16x16x128_f8f6f4 v[110:113], v[206:209], v[8:13], v[110:113], v177, v241 op_sel:[0,1,0] op_sel_hi:[0,0,0] cbsz:4 blgp:2
	v_mfma_scale_f32_16x16x128_f8f6f4 v[98:101], v[210:213], v[8:13], v[98:101], v177, v241 op_sel:[0,1,0] op_sel_hi:[0,0,0] cbsz:4 blgp:2
	v_mfma_scale_f32_16x16x128_f8f6f4 v[82:85], v[214:217], v[8:13], v[82:85], v177, v241 op_sel:[0,1,0] op_sel_hi:[0,0,0] cbsz:4 blgp:2
	v_mfma_scale_f32_16x16x128_f8f6f4 v[66:69], v[218:221], v[8:13], v[66:69], v177, v241 op_sel:[0,1,0] op_sel_hi:[0,0,0] cbsz:4 blgp:2
	v_mfma_scale_f32_16x16x128_f8f6f4 v[50:53], v[222:225], v[8:13], v[50:53], v177, v241 op_sel:[0,1,0] op_sel_hi:[0,0,0] cbsz:4 blgp:2
	v_mfma_scale_f32_16x16x128_f8f6f4 v[34:37], v[226:229], v[8:13], v[34:37], v177, v241 op_sel:[0,1,0] op_sel_hi:[0,0,0] cbsz:4 blgp:2
	v_mfma_scale_f32_16x16x128_f8f6f4 v[106:109], v[202:205], v[14:19], v[106:109], v177, v242 op_sel:[0,1,0] op_sel_hi:[0,0,0] cbsz:4 blgp:2
	v_mfma_scale_f32_16x16x128_f8f6f4 v[94:97], v[206:209], v[14:19], v[94:97], v177, v242 op_sel:[0,1,0] op_sel_hi:[0,0,0] cbsz:4 blgp:2
	v_mfma_scale_f32_16x16x128_f8f6f4 v[78:81], v[210:213], v[14:19], v[78:81], v177, v242 op_sel:[0,1,0] op_sel_hi:[0,0,0] cbsz:4 blgp:2
	v_mfma_scale_f32_16x16x128_f8f6f4 v[62:65], v[214:217], v[14:19], v[62:65], v177, v242 op_sel:[0,1,0] op_sel_hi:[0,0,0] cbsz:4 blgp:2
	v_mfma_scale_f32_16x16x128_f8f6f4 v[46:49], v[218:221], v[14:19], v[46:49], v177, v242 op_sel:[0,1,0] op_sel_hi:[0,0,0] cbsz:4 blgp:2
	v_mfma_scale_f32_16x16x128_f8f6f4 v[30:33], v[222:225], v[14:19], v[30:33], v177, v242 op_sel:[0,1,0] op_sel_hi:[0,0,0] cbsz:4 blgp:2
	v_mfma_scale_f32_16x16x128_f8f6f4 v[90:93], v[202:205], v[20:25], v[90:93], v177, v243 op_sel:[0,1,0] op_sel_hi:[0,0,0] cbsz:4 blgp:2
	v_mfma_scale_f32_16x16x128_f8f6f4 v[74:77], v[206:209], v[20:25], v[74:77], v177, v243 op_sel:[0,1,0] op_sel_hi:[0,0,0] cbsz:4 blgp:2
	v_mfma_scale_f32_16x16x128_f8f6f4 v[58:61], v[210:213], v[20:25], v[58:61], v177, v243 op_sel:[0,1,0] op_sel_hi:[0,0,0] cbsz:4 blgp:2
	v_mfma_scale_f32_16x16x128_f8f6f4 v[42:45], v[214:217], v[20:25], v[42:45], v177, v243 op_sel:[0,1,0] op_sel_hi:[0,0,0] cbsz:4 blgp:2
	v_mfma_scale_f32_16x16x128_f8f6f4 v[26:29], v[218:221], v[20:25], v[26:29], v177, v243 op_sel:[0,1,0] op_sel_hi:[0,0,0] cbsz:4 blgp:2
	v_mfma_scale_f32_16x16x128_f8f6f4 v[178:181], v[230:233], v[8:13], v[178:181], v177, v241 op_sel:[0,1,0] op_sel_hi:[0,0,0] cbsz:4 blgp:2
	v_mfma_scale_f32_16x16x128_f8f6f4 v[182:185], v[226:229], v[14:19], v[182:185], v177, v242 op_sel:[0,1,0] op_sel_hi:[0,0,0] cbsz:4 blgp:2
	v_mfma_scale_f32_16x16x128_f8f6f4 v[186:189], v[230:233], v[14:19], v[186:189], v177, v242 op_sel:[0,1,0] op_sel_hi:[0,0,0] cbsz:4 blgp:2
	v_mfma_scale_f32_16x16x128_f8f6f4 v[190:193], v[222:225], v[20:25], v[190:193], v177, v243 op_sel:[0,1,0] op_sel_hi:[0,0,0] cbsz:4 blgp:2
	v_mfma_scale_f32_16x16x128_f8f6f4 v[198:201], v[226:229], v[20:25], v[234:237], v177, v243 op_sel:[0,1,0] op_sel_hi:[0,0,0] cbsz:4 blgp:2
	v_mfma_scale_f32_16x16x128_f8f6f4 v[194:197], v[230:233], v[20:25], v[194:197], v177, v243 op_sel:[0,1,0] op_sel_hi:[0,0,0] cbsz:4 blgp:2
	s_barrier
	ds_read_b128 v[202:205], v166
	ds_read_b128 v[206:209], v166 offset:256
	ds_read_b128 v[210:213], v166 offset:512
	ds_read_b128 v[214:217], v166 offset:768
	ds_read_b128 v[218:221], v166 offset:1024
	ds_read_b128 v[222:225], v166 offset:1280
	ds_read_b128 v[226:229], v166 offset:1536
	ds_read_b128 v[230:233], v166 offset:1792
	ds_read2_b64 v[2:5], v162 offset1:1
	ds_read2_b64 v[6:9], v162 offset0:2 offset1:48
	ds_read2_b64 v[10:13], v162 offset0:49 offset1:50
	s_mov_b32 m0, s47
	ds_read2_b64 v[14:17], v162 offset0:96 offset1:97
	global_load_lds_dwordx4 v144, s[78:79]
	s_mov_b32 m0, s48
	ds_read2_b64 v[18:21], v162 offset0:98 offset1:144
	global_load_lds_dwordx4 v145, s[78:79]
	s_mov_b32 m0, s49
	ds_read2_b64 v[22:25], v162 offset0:145 offset1:146
	global_load_lds_dwordx4 v146, s[78:79]
	v_add_u32_e32 v234, s44, v176
	ds_read_u16 v242, v234
	ds_read_u16 v243, v234 offset:32
	ds_read_u16 v244, v234 offset:64
	s_and_b32 s44, s62, 0x1000
	s_add_i32 m0, s50, s44
	ds_read_u16 v245, v234 offset:96
	global_load_lds_dword v151, s[80:81]
	s_waitcnt vmcnt(6)
	s_waitcnt lgkmcnt(0)
	s_barrier
	v_mfma_scale_f32_16x16x128_f8f6f4 v[126:129], v[202:205], v[2:7], v[126:129], v177, v242 op_sel_hi:[0,0,0] cbsz:4 blgp:2
	v_mfma_scale_f32_16x16x128_f8f6f4 v[122:125], v[206:209], v[2:7], v[122:125], v177, v242 op_sel_hi:[0,0,0] cbsz:4 blgp:2
	v_mfma_scale_f32_16x16x128_f8f6f4 v[114:117], v[210:213], v[2:7], v[114:117], v177, v242 op_sel_hi:[0,0,0] cbsz:4 blgp:2
	v_mfma_scale_f32_16x16x128_f8f6f4 v[102:105], v[214:217], v[2:7], v[102:105], v177, v242 op_sel_hi:[0,0,0] cbsz:4 blgp:2
	v_mfma_scale_f32_16x16x128_f8f6f4 v[86:89], v[218:221], v[2:7], v[86:89], v177, v242 op_sel_hi:[0,0,0] cbsz:4 blgp:2
	v_mfma_scale_f32_16x16x128_f8f6f4 v[70:73], v[222:225], v[2:7], v[70:73], v177, v242 op_sel_hi:[0,0,0] cbsz:4 blgp:2
	v_mfma_scale_f32_16x16x128_f8f6f4 v[54:57], v[226:229], v[2:7], v[54:57], v177, v242 op_sel_hi:[0,0,0] cbsz:4 blgp:2
	v_mfma_scale_f32_16x16x128_f8f6f4 v[38:41], v[230:233], v[2:7], v[38:41], v177, v242 op_sel_hi:[0,0,0] cbsz:4 blgp:2
	v_mfma_scale_f32_16x16x128_f8f6f4 v[118:121], v[202:205], v[8:13], v[118:121], v177, v243 op_sel_hi:[0,0,0] cbsz:4 blgp:2
	v_mfma_scale_f32_16x16x128_f8f6f4 v[110:113], v[206:209], v[8:13], v[110:113], v177, v243 op_sel_hi:[0,0,0] cbsz:4 blgp:2
	v_mfma_scale_f32_16x16x128_f8f6f4 v[98:101], v[210:213], v[8:13], v[98:101], v177, v243 op_sel_hi:[0,0,0] cbsz:4 blgp:2
	v_mfma_scale_f32_16x16x128_f8f6f4 v[82:85], v[214:217], v[8:13], v[82:85], v177, v243 op_sel_hi:[0,0,0] cbsz:4 blgp:2
	v_mfma_scale_f32_16x16x128_f8f6f4 v[66:69], v[218:221], v[8:13], v[66:69], v177, v243 op_sel_hi:[0,0,0] cbsz:4 blgp:2
	v_mfma_scale_f32_16x16x128_f8f6f4 v[50:53], v[222:225], v[8:13], v[50:53], v177, v243 op_sel_hi:[0,0,0] cbsz:4 blgp:2
	v_mfma_scale_f32_16x16x128_f8f6f4 v[34:37], v[226:229], v[8:13], v[34:37], v177, v243 op_sel_hi:[0,0,0] cbsz:4 blgp:2
	v_mfma_scale_f32_16x16x128_f8f6f4 v[106:109], v[202:205], v[14:19], v[106:109], v177, v244 op_sel_hi:[0,0,0] cbsz:4 blgp:2
	v_mfma_scale_f32_16x16x128_f8f6f4 v[94:97], v[206:209], v[14:19], v[94:97], v177, v244 op_sel_hi:[0,0,0] cbsz:4 blgp:2
	v_mfma_scale_f32_16x16x128_f8f6f4 v[78:81], v[210:213], v[14:19], v[78:81], v177, v244 op_sel_hi:[0,0,0] cbsz:4 blgp:2
	v_mfma_scale_f32_16x16x128_f8f6f4 v[62:65], v[214:217], v[14:19], v[62:65], v177, v244 op_sel_hi:[0,0,0] cbsz:4 blgp:2
	v_mfma_scale_f32_16x16x128_f8f6f4 v[46:49], v[218:221], v[14:19], v[46:49], v177, v244 op_sel_hi:[0,0,0] cbsz:4 blgp:2
	v_mfma_scale_f32_16x16x128_f8f6f4 v[30:33], v[222:225], v[14:19], v[30:33], v177, v244 op_sel_hi:[0,0,0] cbsz:4 blgp:2
	v_mfma_scale_f32_16x16x128_f8f6f4 v[238:241], v[226:229], v[14:19], v[182:185], v177, v244 op_sel_hi:[0,0,0] cbsz:4 blgp:2
	v_mfma_scale_f32_16x16x128_f8f6f4 v[14:17], v[230:233], v[14:19], v[186:189], v177, v244 op_sel_hi:[0,0,0] cbsz:4 blgp:2
	v_mfma_scale_f32_16x16x128_f8f6f4 v[90:93], v[202:205], v[20:25], v[90:93], v177, v245 op_sel_hi:[0,0,0] cbsz:4 blgp:2
	v_mfma_scale_f32_16x16x128_f8f6f4 v[74:77], v[206:209], v[20:25], v[74:77], v177, v245 op_sel_hi:[0,0,0] cbsz:4 blgp:2
	v_mfma_scale_f32_16x16x128_f8f6f4 v[58:61], v[210:213], v[20:25], v[58:61], v177, v245 op_sel_hi:[0,0,0] cbsz:4 blgp:2
	v_mfma_scale_f32_16x16x128_f8f6f4 v[42:45], v[214:217], v[20:25], v[42:45], v177, v245 op_sel_hi:[0,0,0] cbsz:4 blgp:2
	v_mfma_scale_f32_16x16x128_f8f6f4 v[26:29], v[218:221], v[20:25], v[26:29], v177, v245 op_sel_hi:[0,0,0] cbsz:4 blgp:2
	v_mfma_scale_f32_16x16x128_f8f6f4 v[234:237], v[230:233], v[8:13], v[178:181], v177, v243 op_sel_hi:[0,0,0] cbsz:4 blgp:2
	v_mfma_scale_f32_16x16x128_f8f6f4 v[190:193], v[222:225], v[20:25], v[190:193], v177, v245 op_sel_hi:[0,0,0] cbsz:4 blgp:2
	v_mfma_scale_f32_16x16x128_f8f6f4 v[198:201], v[226:229], v[20:25], v[198:201], v177, v245 op_sel_hi:[0,0,0] cbsz:4 blgp:2
	v_mfma_scale_f32_16x16x128_f8f6f4 v[194:197], v[230:233], v[20:25], v[194:197], v177, v245 op_sel_hi:[0,0,0] cbsz:4 blgp:2
	s_barrier
	ds_read2_b64 v[2:5], v1 offset1:1
	s_mov_b32 m0, s53
	ds_read2_b64 v[6:9], v1 offset0:2 offset1:48
	global_load_lds_dwordx4 v147, s[78:79]
	s_mov_b32 m0, s55
	ds_read2_b64 v[10:13], v1 offset0:49 offset1:50
	global_load_lds_dwordx4 v148, s[78:79]
	s_mov_b32 m0, s56
	ds_read2_b64 v[178:181], v159 offset1:1
	global_load_lds_dwordx4 v149, s[78:79]
	s_mov_b32 m0, s63
	ds_read2_b64 v[182:185], v159 offset0:2 offset1:48
	global_load_lds_dwordx4 v142, s[74:75]
	s_mov_b32 m0, s60
	ds_read2_b64 v[186:189], v159 offset0:49 offset1:50
	global_load_lds_dwordx4 v143, s[74:75]
	s_waitcnt vmcnt(5)
	s_waitcnt lgkmcnt(0)
	s_barrier
	v_mfma_scale_f32_16x16x128_f8f6f4 v[126:129], v[202:205], v[2:7], v[126:129], v177, v242 op_sel:[0,1,0] op_sel_hi:[0,0,0] cbsz:4 blgp:2
	v_mfma_scale_f32_16x16x128_f8f6f4 v[122:125], v[206:209], v[2:7], v[122:125], v177, v242 op_sel:[0,1,0] op_sel_hi:[0,0,0] cbsz:4 blgp:2
	v_mfma_scale_f32_16x16x128_f8f6f4 v[114:117], v[210:213], v[2:7], v[114:117], v177, v242 op_sel:[0,1,0] op_sel_hi:[0,0,0] cbsz:4 blgp:2
	v_mfma_scale_f32_16x16x128_f8f6f4 v[102:105], v[214:217], v[2:7], v[102:105], v177, v242 op_sel:[0,1,0] op_sel_hi:[0,0,0] cbsz:4 blgp:2
	v_mfma_scale_f32_16x16x128_f8f6f4 v[86:89], v[218:221], v[2:7], v[86:89], v177, v242 op_sel:[0,1,0] op_sel_hi:[0,0,0] cbsz:4 blgp:2
	v_mfma_scale_f32_16x16x128_f8f6f4 v[70:73], v[222:225], v[2:7], v[70:73], v177, v242 op_sel:[0,1,0] op_sel_hi:[0,0,0] cbsz:4 blgp:2
	v_mfma_scale_f32_16x16x128_f8f6f4 v[54:57], v[226:229], v[2:7], v[54:57], v177, v242 op_sel:[0,1,0] op_sel_hi:[0,0,0] cbsz:4 blgp:2
	v_mfma_scale_f32_16x16x128_f8f6f4 v[38:41], v[230:233], v[2:7], v[38:41], v177, v242 op_sel:[0,1,0] op_sel_hi:[0,0,0] cbsz:4 blgp:2
	v_mfma_scale_f32_16x16x128_f8f6f4 v[118:121], v[202:205], v[8:13], v[118:121], v177, v243 op_sel:[0,1,0] op_sel_hi:[0,0,0] cbsz:4 blgp:2
	v_mfma_scale_f32_16x16x128_f8f6f4 v[110:113], v[206:209], v[8:13], v[110:113], v177, v243 op_sel:[0,1,0] op_sel_hi:[0,0,0] cbsz:4 blgp:2
	v_mfma_scale_f32_16x16x128_f8f6f4 v[98:101], v[210:213], v[8:13], v[98:101], v177, v243 op_sel:[0,1,0] op_sel_hi:[0,0,0] cbsz:4 blgp:2
	v_mfma_scale_f32_16x16x128_f8f6f4 v[82:85], v[214:217], v[8:13], v[82:85], v177, v243 op_sel:[0,1,0] op_sel_hi:[0,0,0] cbsz:4 blgp:2
	v_mfma_scale_f32_16x16x128_f8f6f4 v[66:69], v[218:221], v[8:13], v[66:69], v177, v243 op_sel:[0,1,0] op_sel_hi:[0,0,0] cbsz:4 blgp:2
	v_mfma_scale_f32_16x16x128_f8f6f4 v[50:53], v[222:225], v[8:13], v[50:53], v177, v243 op_sel:[0,1,0] op_sel_hi:[0,0,0] cbsz:4 blgp:2
	v_mfma_scale_f32_16x16x128_f8f6f4 v[34:37], v[226:229], v[8:13], v[34:37], v177, v243 op_sel:[0,1,0] op_sel_hi:[0,0,0] cbsz:4 blgp:2
	v_mfma_scale_f32_16x16x128_f8f6f4 v[22:25], v[230:233], v[8:13], v[234:237], v177, v243 op_sel:[0,1,0] op_sel_hi:[0,0,0] cbsz:4 blgp:2
	v_mfma_scale_f32_16x16x128_f8f6f4 v[106:109], v[202:205], v[178:183], v[106:109], v177, v244 op_sel:[0,1,0] op_sel_hi:[0,0,0] cbsz:4 blgp:2
	v_mfma_scale_f32_16x16x128_f8f6f4 v[94:97], v[206:209], v[178:183], v[94:97], v177, v244 op_sel:[0,1,0] op_sel_hi:[0,0,0] cbsz:4 blgp:2
	v_mfma_scale_f32_16x16x128_f8f6f4 v[78:81], v[210:213], v[178:183], v[78:81], v177, v244 op_sel:[0,1,0] op_sel_hi:[0,0,0] cbsz:4 blgp:2
	v_mfma_scale_f32_16x16x128_f8f6f4 v[62:65], v[214:217], v[178:183], v[62:65], v177, v244 op_sel:[0,1,0] op_sel_hi:[0,0,0] cbsz:4 blgp:2
	v_mfma_scale_f32_16x16x128_f8f6f4 v[46:49], v[218:221], v[178:183], v[46:49], v177, v244 op_sel:[0,1,0] op_sel_hi:[0,0,0] cbsz:4 blgp:2
	v_mfma_scale_f32_16x16x128_f8f6f4 v[30:33], v[222:225], v[178:183], v[30:33], v177, v244 op_sel:[0,1,0] op_sel_hi:[0,0,0] cbsz:4 blgp:2
	v_mfma_scale_f32_16x16x128_f8f6f4 v[18:21], v[226:229], v[178:183], v[238:241], v177, v244 op_sel:[0,1,0] op_sel_hi:[0,0,0] cbsz:4 blgp:2
	v_mfma_scale_f32_16x16x128_f8f6f4 v[10:13], v[230:233], v[178:183], v[14:17], v177, v244 op_sel:[0,1,0] op_sel_hi:[0,0,0] cbsz:4 blgp:2
	v_mfma_scale_f32_16x16x128_f8f6f4 v[90:93], v[202:205], v[184:189], v[90:93], v177, v245 op_sel:[0,1,0] op_sel_hi:[0,0,0] cbsz:4 blgp:2
	v_mfma_scale_f32_16x16x128_f8f6f4 v[74:77], v[206:209], v[184:189], v[74:77], v177, v245 op_sel:[0,1,0] op_sel_hi:[0,0,0] cbsz:4 blgp:2
	v_mfma_scale_f32_16x16x128_f8f6f4 v[58:61], v[210:213], v[184:189], v[58:61], v177, v245 op_sel:[0,1,0] op_sel_hi:[0,0,0] cbsz:4 blgp:2
	v_mfma_scale_f32_16x16x128_f8f6f4 v[42:45], v[214:217], v[184:189], v[42:45], v177, v245 op_sel:[0,1,0] op_sel_hi:[0,0,0] cbsz:4 blgp:2
	v_mfma_scale_f32_16x16x128_f8f6f4 v[26:29], v[218:221], v[184:189], v[26:29], v177, v245 op_sel:[0,1,0] op_sel_hi:[0,0,0] cbsz:4 blgp:2
	v_mfma_scale_f32_16x16x128_f8f6f4 v[14:17], v[222:225], v[184:189], v[190:193], v177, v245 op_sel:[0,1,0] op_sel_hi:[0,0,0] cbsz:4 blgp:2
	v_mfma_scale_f32_16x16x128_f8f6f4 v[6:9], v[226:229], v[184:189], v[198:201], v177, v245 op_sel:[0,1,0] op_sel_hi:[0,0,0] cbsz:4 blgp:2
	v_mfma_scale_f32_16x16x128_f8f6f4 v[2:5], v[230:233], v[184:189], v[194:197], v177, v245 op_sel:[0,1,0] op_sel_hi:[0,0,0] cbsz:4 blgp:2
	s_barrier
	s_add_i32 s61, s61, 2
	s_addk_i32 s62, 0x1000
	s_add_u32 s72, s72, 0x8000
	s_addc_u32 s73, s73, 0
	s_add_u32 s74, s74, 0x8000
	s_addc_u32 s75, s75, 0
	s_add_u32 s76, s76, 0x18000
	s_addc_u32 s77, s77, 0
	s_add_u32 s78, s78, 0x18000
	s_addc_u32 s79, s79, 0
	s_add_u32 s80, s80, 0x1000
	s_addc_u32 s81, s81, 0
	s_cmp_lt_u32 s61, 4
	s_cbranch_scc1 .LBB2_3
	ds_read_b128 v[154:157], v175
	ds_read_b128 v[186:189], v175 offset:256
	ds_read_b128 v[190:193], v175 offset:512
	ds_read_b128 v[194:197], v175 offset:768
	ds_read_b128 v[198:201], v175 offset:1024
	ds_read_b128 v[202:205], v175 offset:1280
	ds_read_b128 v[206:209], v175 offset:1536
	ds_read_b128 v[210:213], v175 offset:1792
	ds_read_b64 v[142:143], v171
	ds_read_b64 v[144:145], v171 offset:8
	ds_read_b64 v[146:147], v171 offset:16
	ds_read_b64 v[148:149], v174
	ds_read_b64 v[150:151], v174 offset:8
	ds_read_b64 v[152:153], v174 offset:16
	ds_read_b64 v[174:175], v173
	ds_read_b64 v[176:177], v173 offset:8
	ds_read_b64 v[178:179], v173 offset:16
	ds_read_b64 v[180:181], v172
	ds_read_b64 v[182:183], v172 offset:8
	ds_read_b64 v[184:185], v172 offset:16
	v_add_u32_e32 v171, 0x21000, v161
	v_add_u32_e32 v172, 0x21020, v161
	v_add_u32_e32 v173, 0x21040, v161
	v_add_u32_e32 v214, 0x21060, v161
	s_mov_b64 s[0:1], 0x1c000
	s_mov_b32 m0, s63
	ds_read_u16 v171, v171
	ds_read_u16 v215, v172
	ds_read_u16 v216, v173
	ds_read_u16 v214, v214
	v_lshl_add_u64 v[172:173], v[138:139], 0, s[0:1]
	s_mov_b64 s[0:1], 0x1e000
	v_lshl_add_u64 v[138:139], v[138:139], 0, s[0:1]
	s_mov_b32 m0, s60
	s_mov_b64 s[0:1], 0x54000
	v_lshl_add_u64 v[138:139], v[140:141], 0, s[0:1]
	v_lshl_add_u64 v[140:141], v[138:139], 0, s[18:19]
	s_mov_b32 m0, s59
	v_lshl_add_u64 v[130:131], s[16:17], 0, v[130:131]
	global_load_lds_dwordx4 v[140:141], off
	v_lshl_add_u64 v[140:141], v[138:139], 0, s[20:21]
	s_mov_b32 m0, s58
	v_lshl_add_u64 v[138:139], v[138:139], 0, s[22:23]
	global_load_lds_dwordx4 v[140:141], off
	s_mov_b32 m0, s57
	s_mov_b64 s[0:1], 0x3800
	global_load_lds_dwordx4 v[138:139], off
	v_lshl_add_u64 v[130:131], v[130:131], 0, s[0:1]
	s_add_i32 m0, s3, 0x21800
	s_waitcnt lgkmcnt(0)
	v_mov_b32_e32 v172, v216
	global_load_lds_dword v[130:131], off
	s_waitcnt vmcnt(6)
	s_waitcnt lgkmcnt(0)
	v_mov_b32_e32 v130, v171
	v_mov_b32_e32 v131, v215
	v_mov_b32_e32 v217, v214
	s_barrier
	v_mov_b32_e32 v240, 0x7f7f7f7f
	s_nop 1
	v_mfma_scale_f32_16x16x128_f8f6f4 v[126:129], v[154:157], v[142:147], v[126:129], v240, v130 op_sel_hi:[0,0,0] cbsz:4 blgp:2
	v_mfma_scale_f32_16x16x128_f8f6f4 v[122:125], v[186:189], v[142:147], v[122:125], v240, v130 op_sel_hi:[0,0,0] cbsz:4 blgp:2
	v_mfma_scale_f32_16x16x128_f8f6f4 v[114:117], v[190:193], v[142:147], v[114:117], v240, v130 op_sel_hi:[0,0,0] cbsz:4 blgp:2
	v_mfma_scale_f32_16x16x128_f8f6f4 v[102:105], v[194:197], v[142:147], v[102:105], v240, v130 op_sel_hi:[0,0,0] cbsz:4 blgp:2
	v_mfma_scale_f32_16x16x128_f8f6f4 v[86:89], v[198:201], v[142:147], v[86:89], v240, v130 op_sel_hi:[0,0,0] cbsz:4 blgp:2
	v_mfma_scale_f32_16x16x128_f8f6f4 v[70:73], v[202:205], v[142:147], v[70:73], v240, v130 op_sel_hi:[0,0,0] cbsz:4 blgp:2
	v_mfma_scale_f32_16x16x128_f8f6f4 v[54:57], v[206:209], v[142:147], v[54:57], v240, v130 op_sel_hi:[0,0,0] cbsz:4 blgp:2
	v_mfma_scale_f32_16x16x128_f8f6f4 v[38:41], v[210:213], v[142:147], v[38:41], v240, v130 op_sel_hi:[0,0,0] cbsz:4 blgp:2
	v_mfma_scale_f32_16x16x128_f8f6f4 v[118:121], v[154:157], v[148:153], v[118:121], v240, v131 op_sel_hi:[0,0,0] cbsz:4 blgp:2
	v_mfma_scale_f32_16x16x128_f8f6f4 v[110:113], v[186:189], v[148:153], v[110:113], v240, v131 op_sel_hi:[0,0,0] cbsz:4 blgp:2
	v_mfma_scale_f32_16x16x128_f8f6f4 v[98:101], v[190:193], v[148:153], v[98:101], v240, v131 op_sel_hi:[0,0,0] cbsz:4 blgp:2
	v_mfma_scale_f32_16x16x128_f8f6f4 v[82:85], v[194:197], v[148:153], v[82:85], v240, v131 op_sel_hi:[0,0,0] cbsz:4 blgp:2
	v_mfma_scale_f32_16x16x128_f8f6f4 v[66:69], v[198:201], v[148:153], v[66:69], v240, v131 op_sel_hi:[0,0,0] cbsz:4 blgp:2
	v_mfma_scale_f32_16x16x128_f8f6f4 v[50:53], v[202:205], v[148:153], v[50:53], v240, v131 op_sel_hi:[0,0,0] cbsz:4 blgp:2
	v_mfma_scale_f32_16x16x128_f8f6f4 v[138:141], v[210:213], v[148:153], v[22:25], v240, v131 op_sel_hi:[0,0,0] cbsz:4 blgp:2
	v_mfma_scale_f32_16x16x128_f8f6f4 v[106:109], v[154:157], v[174:179], v[106:109], v240, v172 op_sel_hi:[0,0,0] cbsz:4 blgp:2
	v_mfma_scale_f32_16x16x128_f8f6f4 v[94:97], v[186:189], v[174:179], v[94:97], v240, v172 op_sel_hi:[0,0,0] cbsz:4 blgp:2
	v_mfma_scale_f32_16x16x128_f8f6f4 v[78:81], v[190:193], v[174:179], v[78:81], v240, v172 op_sel_hi:[0,0,0] cbsz:4 blgp:2
	v_mfma_scale_f32_16x16x128_f8f6f4 v[62:65], v[194:197], v[174:179], v[62:65], v240, v172 op_sel_hi:[0,0,0] cbsz:4 blgp:2
	v_mfma_scale_f32_16x16x128_f8f6f4 v[46:49], v[198:201], v[174:179], v[46:49], v240, v172 op_sel_hi:[0,0,0] cbsz:4 blgp:2
	v_mfma_scale_f32_16x16x128_f8f6f4 v[30:33], v[202:205], v[174:179], v[30:33], v240, v172 op_sel_hi:[0,0,0] cbsz:4 blgp:2
	v_mfma_scale_f32_16x16x128_f8f6f4 v[142:145], v[206:209], v[174:179], v[18:21], v240, v172 op_sel_hi:[0,0,0] cbsz:4 blgp:2
	v_mfma_scale_f32_16x16x128_f8f6f4 v[90:93], v[154:157], v[180:185], v[90:93], v240, v217 op_sel_hi:[0,0,0] cbsz:4 blgp:2
	v_mfma_scale_f32_16x16x128_f8f6f4 v[74:77], v[186:189], v[180:185], v[74:77], v240, v217 op_sel_hi:[0,0,0] cbsz:4 blgp:2
	v_mfma_scale_f32_16x16x128_f8f6f4 v[58:61], v[190:193], v[180:185], v[58:61], v240, v217 op_sel_hi:[0,0,0] cbsz:4 blgp:2
	v_mfma_scale_f32_16x16x128_f8f6f4 v[26:29], v[198:201], v[180:185], v[26:29], v240, v217 op_sel_hi:[0,0,0] cbsz:4 blgp:2
	v_mfma_scale_f32_16x16x128_f8f6f4 v[34:37], v[206:209], v[148:153], v[34:37], v240, v131 op_sel_hi:[0,0,0] cbsz:4 blgp:2
	v_mfma_scale_f32_16x16x128_f8f6f4 v[146:149], v[210:213], v[174:179], v[10:13], v240, v172 op_sel_hi:[0,0,0] cbsz:4 blgp:2
	v_mfma_scale_f32_16x16x128_f8f6f4 v[42:45], v[194:197], v[180:185], v[42:45], v240, v217 op_sel_hi:[0,0,0] cbsz:4 blgp:2
	v_mfma_scale_f32_16x16x128_f8f6f4 v[150:153], v[202:205], v[180:185], v[14:17], v240, v217 op_sel_hi:[0,0,0] cbsz:4 blgp:2
	v_mfma_scale_f32_16x16x128_f8f6f4 v[172:175], v[206:209], v[180:185], v[6:9], v240, v217 op_sel_hi:[0,0,0] cbsz:4 blgp:2
	v_mfma_scale_f32_16x16x128_f8f6f4 v[176:179], v[210:213], v[180:185], v[2:5], v240, v217 op_sel_hi:[0,0,0] cbsz:4 blgp:2
	s_barrier
	ds_read_b64 v[2:3], v167
	ds_read_b64 v[4:5], v167 offset:8
	ds_read_b64 v[6:7], v167 offset:16
	ds_read_b64 v[8:9], v170
	ds_read_b64 v[10:11], v170 offset:8
	ds_read_b64 v[12:13], v170 offset:16
	ds_read_b64 v[14:15], v169
	ds_read_b64 v[16:17], v169 offset:8
	ds_read_b64 v[18:19], v169 offset:16
	s_mov_b64 s[0:1], 0x55800
	s_mov_b32 m0, s54
	ds_read_b64 v[20:21], v168
	ds_read_b64 v[22:23], v168 offset:8
	ds_read_b64 v[24:25], v168 offset:16
	v_lshl_add_u64 v[130:131], v[132:133], 0, s[0:1]
	global_load_lds_dwordx4 v[130:131], off
	v_lshl_add_u64 v[130:131], v[134:135], 0, s[0:1]
	s_mov_b32 m0, s52
	v_lshrrev_b32_e32 v167, 8, v216
	global_load_lds_dwordx4 v[130:131], off
	v_lshl_add_u64 v[130:131], v[136:137], 0, s[0:1]
	s_mov_b32 m0, s51
	v_lshrrev_b32_e32 v168, 8, v214
	global_load_lds_dwordx4 v[130:131], off
	s_waitcnt vmcnt(3)
	s_waitcnt lgkmcnt(0)
	v_lshrrev_b32_e32 v130, 8, v171
	v_lshrrev_b32_e32 v131, 8, v215
	s_barrier
	v_mfma_scale_f32_16x16x128_f8f6f4 v[126:129], v[154:157], v[2:7], v[126:129], v240, v130 op_sel_hi:[0,0,0] cbsz:4 blgp:2
	v_mfma_scale_f32_16x16x128_f8f6f4 v[122:125], v[186:189], v[2:7], v[122:125], v240, v130 op_sel_hi:[0,0,0] cbsz:4 blgp:2
	v_mfma_scale_f32_16x16x128_f8f6f4 v[114:117], v[190:193], v[2:7], v[114:117], v240, v130 op_sel_hi:[0,0,0] cbsz:4 blgp:2
	v_mfma_scale_f32_16x16x128_f8f6f4 v[102:105], v[194:197], v[2:7], v[102:105], v240, v130 op_sel_hi:[0,0,0] cbsz:4 blgp:2
	v_mfma_scale_f32_16x16x128_f8f6f4 v[86:89], v[198:201], v[2:7], v[86:89], v240, v130 op_sel_hi:[0,0,0] cbsz:4 blgp:2
	v_mfma_scale_f32_16x16x128_f8f6f4 v[70:73], v[202:205], v[2:7], v[70:73], v240, v130 op_sel_hi:[0,0,0] cbsz:4 blgp:2
	v_mfma_scale_f32_16x16x128_f8f6f4 v[54:57], v[206:209], v[2:7], v[54:57], v240, v130 op_sel_hi:[0,0,0] cbsz:4 blgp:2
	v_mfma_scale_f32_16x16x128_f8f6f4 v[38:41], v[210:213], v[2:7], v[38:41], v240, v130 op_sel_hi:[0,0,0] cbsz:4 blgp:2
	v_mfma_scale_f32_16x16x128_f8f6f4 v[118:121], v[154:157], v[8:13], v[118:121], v240, v131 op_sel_hi:[0,0,0] cbsz:4 blgp:2
	v_mfma_scale_f32_16x16x128_f8f6f4 v[110:113], v[186:189], v[8:13], v[110:113], v240, v131 op_sel_hi:[0,0,0] cbsz:4 blgp:2
	v_mfma_scale_f32_16x16x128_f8f6f4 v[98:101], v[190:193], v[8:13], v[98:101], v240, v131 op_sel_hi:[0,0,0] cbsz:4 blgp:2
	v_mfma_scale_f32_16x16x128_f8f6f4 v[82:85], v[194:197], v[8:13], v[82:85], v240, v131 op_sel_hi:[0,0,0] cbsz:4 blgp:2
	v_mfma_scale_f32_16x16x128_f8f6f4 v[66:69], v[198:201], v[8:13], v[66:69], v240, v131 op_sel_hi:[0,0,0] cbsz:4 blgp:2
	v_mfma_scale_f32_16x16x128_f8f6f4 v[50:53], v[202:205], v[8:13], v[50:53], v240, v131 op_sel_hi:[0,0,0] cbsz:4 blgp:2
	v_mfma_scale_f32_16x16x128_f8f6f4 v[34:37], v[206:209], v[8:13], v[34:37], v240, v131 op_sel_hi:[0,0,0] cbsz:4 blgp:2
	v_mfma_scale_f32_16x16x128_f8f6f4 v[130:133], v[210:213], v[8:13], v[138:141], v240, v131 op_sel_hi:[0,0,0] cbsz:4 blgp:2
	v_mfma_scale_f32_16x16x128_f8f6f4 v[106:109], v[154:157], v[14:19], v[106:109], v240, v167 op_sel_hi:[0,0,0] cbsz:4 blgp:2
	v_mfma_scale_f32_16x16x128_f8f6f4 v[94:97], v[186:189], v[14:19], v[94:97], v240, v167 op_sel_hi:[0,0,0] cbsz:4 blgp:2
	v_mfma_scale_f32_16x16x128_f8f6f4 v[78:81], v[190:193], v[14:19], v[78:81], v240, v167 op_sel_hi:[0,0,0] cbsz:4 blgp:2
	v_mfma_scale_f32_16x16x128_f8f6f4 v[62:65], v[194:197], v[14:19], v[62:65], v240, v167 op_sel_hi:[0,0,0] cbsz:4 blgp:2
	v_mfma_scale_f32_16x16x128_f8f6f4 v[46:49], v[198:201], v[14:19], v[46:49], v240, v167 op_sel_hi:[0,0,0] cbsz:4 blgp:2
	v_mfma_scale_f32_16x16x128_f8f6f4 v[30:33], v[202:205], v[14:19], v[30:33], v240, v167 op_sel_hi:[0,0,0] cbsz:4 blgp:2
	v_mfma_scale_f32_16x16x128_f8f6f4 v[134:137], v[206:209], v[14:19], v[142:145], v240, v167 op_sel_hi:[0,0,0] cbsz:4 blgp:2
	v_mfma_scale_f32_16x16x128_f8f6f4 v[138:141], v[210:213], v[14:19], v[146:149], v240, v167 op_sel_hi:[0,0,0] cbsz:4 blgp:2
	v_mfma_scale_f32_16x16x128_f8f6f4 v[90:93], v[154:157], v[20:25], v[90:93], v240, v168 op_sel_hi:[0,0,0] cbsz:4 blgp:2
	v_mfma_scale_f32_16x16x128_f8f6f4 v[74:77], v[186:189], v[20:25], v[74:77], v240, v168 op_sel_hi:[0,0,0] cbsz:4 blgp:2
	v_mfma_scale_f32_16x16x128_f8f6f4 v[58:61], v[190:193], v[20:25], v[58:61], v240, v168 op_sel_hi:[0,0,0] cbsz:4 blgp:2
	v_mfma_scale_f32_16x16x128_f8f6f4 v[26:29], v[198:201], v[20:25], v[26:29], v240, v168 op_sel_hi:[0,0,0] cbsz:4 blgp:2
	v_mfma_scale_f32_16x16x128_f8f6f4 v[142:145], v[202:205], v[20:25], v[150:153], v240, v168 op_sel_hi:[0,0,0] cbsz:4 blgp:2
	v_mfma_scale_f32_16x16x128_f8f6f4 v[42:45], v[194:197], v[20:25], v[42:45], v240, v168 op_sel_hi:[0,0,0] cbsz:4 blgp:2
	v_mfma_scale_f32_16x16x128_f8f6f4 v[146:149], v[206:209], v[20:25], v[172:175], v240, v168 op_sel_hi:[0,0,0] cbsz:4 blgp:2
	v_mfma_scale_f32_16x16x128_f8f6f4 v[150:153], v[210:213], v[20:25], v[176:179], v240, v168 op_sel_hi:[0,0,0] cbsz:4 blgp:2
	s_barrier
	ds_read_b128 v[154:157], v166
	ds_read_b128 v[168:171], v166 offset:256
	ds_read_b128 v[172:175], v166 offset:512
	ds_read_b128 v[176:179], v166 offset:768
	ds_read_b128 v[180:183], v166 offset:1024
	ds_read_b128 v[184:187], v166 offset:1280
	ds_read_b128 v[188:191], v166 offset:1536
	ds_read_b128 v[192:195], v166 offset:1792
	ds_read_b64 v[2:3], v162
	ds_read_b64 v[4:5], v162 offset:8
	ds_read_b64 v[6:7], v162 offset:16
	ds_read_b64 v[8:9], v165
	ds_read_b64 v[10:11], v165 offset:8
	ds_read_b64 v[12:13], v165 offset:16
	ds_read_b64 v[14:15], v164
	ds_read_b64 v[16:17], v164 offset:8
	ds_read_b64 v[18:19], v164 offset:16
	ds_read_b64 v[20:21], v163
	ds_read_b64 v[22:23], v163 offset:8
	ds_read_b64 v[24:25], v163 offset:16
	v_add_u32_e32 v162, 0x21800, v161
	v_add_u32_e32 v163, 0x21820, v161
	v_add_u32_e32 v164, 0x21840, v161
	v_add_u32_e32 v161, 0x21860, v161
	ds_read_u16 v166, v162
	ds_read_u16 v167, v163
	ds_read_u16 v241, v164
	ds_read_u16 v161, v161
	s_waitcnt vmcnt(0)
	s_waitcnt lgkmcnt(0)
	s_waitcnt lgkmcnt(0)
	v_mov_b32_e32 v162, v166
	v_mov_b32_e32 v200, v167
	v_mov_b32_e32 v216, v241
	v_mov_b32_e32 v242, v161
	s_barrier
	v_mfma_scale_f32_16x16x128_f8f6f4 v[126:129], v[154:157], v[2:7], v[126:129], v240, v162 op_sel_hi:[0,0,0] cbsz:4 blgp:2
	v_mfma_scale_f32_16x16x128_f8f6f4 v[122:125], v[168:171], v[2:7], v[122:125], v240, v162 op_sel_hi:[0,0,0] cbsz:4 blgp:2
	v_mfma_scale_f32_16x16x128_f8f6f4 v[114:117], v[172:175], v[2:7], v[114:117], v240, v162 op_sel_hi:[0,0,0] cbsz:4 blgp:2
	v_mfma_scale_f32_16x16x128_f8f6f4 v[102:105], v[176:179], v[2:7], v[102:105], v240, v162 op_sel_hi:[0,0,0] cbsz:4 blgp:2
	v_mfma_scale_f32_16x16x128_f8f6f4 v[86:89], v[180:183], v[2:7], v[86:89], v240, v162 op_sel_hi:[0,0,0] cbsz:4 blgp:2
	v_mfma_scale_f32_16x16x128_f8f6f4 v[70:73], v[184:187], v[2:7], v[70:73], v240, v162 op_sel_hi:[0,0,0] cbsz:4 blgp:2
	v_mfma_scale_f32_16x16x128_f8f6f4 v[54:57], v[188:191], v[2:7], v[54:57], v240, v162 op_sel_hi:[0,0,0] cbsz:4 blgp:2
	v_mfma_scale_f32_16x16x128_f8f6f4 v[2:5], v[192:195], v[2:7], v[38:41], v240, v162 op_sel_hi:[0,0,0] cbsz:4 blgp:2
	v_mfma_scale_f32_16x16x128_f8f6f4 v[118:121], v[154:157], v[8:13], v[118:121], v240, v200 op_sel_hi:[0,0,0] cbsz:4 blgp:2
	v_mfma_scale_f32_16x16x128_f8f6f4 v[110:113], v[168:171], v[8:13], v[110:113], v240, v200 op_sel_hi:[0,0,0] cbsz:4 blgp:2
	v_mfma_scale_f32_16x16x128_f8f6f4 v[98:101], v[172:175], v[8:13], v[98:101], v240, v200 op_sel_hi:[0,0,0] cbsz:4 blgp:2
	v_mfma_scale_f32_16x16x128_f8f6f4 v[82:85], v[176:179], v[8:13], v[82:85], v240, v200 op_sel_hi:[0,0,0] cbsz:4 blgp:2
	v_mfma_scale_f32_16x16x128_f8f6f4 v[66:69], v[180:183], v[8:13], v[66:69], v240, v200 op_sel_hi:[0,0,0] cbsz:4 blgp:2
	v_mfma_scale_f32_16x16x128_f8f6f4 v[106:109], v[154:157], v[14:19], v[106:109], v240, v216 op_sel_hi:[0,0,0] cbsz:4 blgp:2
	v_mfma_scale_f32_16x16x128_f8f6f4 v[94:97], v[168:171], v[14:19], v[94:97], v240, v216 op_sel_hi:[0,0,0] cbsz:4 blgp:2
	v_mfma_scale_f32_16x16x128_f8f6f4 v[78:81], v[172:175], v[14:19], v[78:81], v240, v216 op_sel_hi:[0,0,0] cbsz:4 blgp:2
	v_mfma_scale_f32_16x16x128_f8f6f4 v[62:65], v[176:179], v[14:19], v[62:65], v240, v216 op_sel_hi:[0,0,0] cbsz:4 blgp:2
	v_mfma_scale_f32_16x16x128_f8f6f4 v[74:77], v[168:171], v[20:25], v[74:77], v240, v242 op_sel_hi:[0,0,0] cbsz:4 blgp:2
	v_mfma_scale_f32_16x16x128_f8f6f4 v[58:61], v[172:175], v[20:25], v[58:61], v240, v242 op_sel_hi:[0,0,0] cbsz:4 blgp:2
	v_mfma_scale_f32_16x16x128_f8f6f4 v[162:165], v[184:187], v[8:13], v[50:53], v240, v200 op_sel_hi:[0,0,0] cbsz:4 blgp:2
	v_mfma_scale_f32_16x16x128_f8f6f4 v[196:199], v[188:191], v[8:13], v[34:37], v240, v200 op_sel_hi:[0,0,0] cbsz:4 blgp:2
	v_mfma_scale_f32_16x16x128_f8f6f4 v[200:203], v[192:195], v[8:13], v[130:133], v240, v200 op_sel_hi:[0,0,0] cbsz:4 blgp:2
	v_mfma_scale_f32_16x16x128_f8f6f4 v[204:207], v[180:183], v[14:19], v[46:49], v240, v216 op_sel_hi:[0,0,0] cbsz:4 blgp:2
	v_mfma_scale_f32_16x16x128_f8f6f4 v[208:211], v[184:187], v[14:19], v[30:33], v240, v216 op_sel_hi:[0,0,0] cbsz:4 blgp:2
	v_mfma_scale_f32_16x16x128_f8f6f4 v[212:215], v[188:191], v[14:19], v[134:137], v240, v216 op_sel_hi:[0,0,0] cbsz:4 blgp:2
	v_mfma_scale_f32_16x16x128_f8f6f4 v[216:219], v[192:195], v[14:19], v[138:141], v240, v216 op_sel_hi:[0,0,0] cbsz:4 blgp:2
	v_mfma_scale_f32_16x16x128_f8f6f4 v[220:223], v[154:157], v[20:25], v[90:93], v240, v242 op_sel_hi:[0,0,0] cbsz:4 blgp:2
	v_mfma_scale_f32_16x16x128_f8f6f4 v[224:227], v[176:179], v[20:25], v[42:45], v240, v242 op_sel_hi:[0,0,0] cbsz:4 blgp:2
	v_mfma_scale_f32_16x16x128_f8f6f4 v[228:231], v[180:183], v[20:25], v[26:29], v240, v242 op_sel_hi:[0,0,0] cbsz:4 blgp:2
	v_mfma_scale_f32_16x16x128_f8f6f4 v[232:235], v[184:187], v[20:25], v[142:145], v240, v242 op_sel_hi:[0,0,0] cbsz:4 blgp:2
	v_mfma_scale_f32_16x16x128_f8f6f4 v[236:239], v[188:191], v[20:25], v[146:149], v240, v242 op_sel_hi:[0,0,0] cbsz:4 blgp:2
	v_mfma_scale_f32_16x16x128_f8f6f4 v[150:153], v[192:195], v[20:25], v[150:153], v240, v242 op_sel_hi:[0,0,0] cbsz:4 blgp:2
	s_barrier
	ds_read_b64 v[34:35], v1
	ds_read_b64 v[36:37], v1 offset:8
	ds_read_b64 v[38:39], v1 offset:16
	ds_read_b64 v[40:41], v160
	ds_read_b64 v[42:43], v160 offset:8
	ds_read_b64 v[44:45], v160 offset:16
	ds_read_b64 v[46:47], v159
	ds_read_b64 v[48:49], v159 offset:8
	ds_read_b64 v[50:51], v159 offset:16
	ds_read_b64 v[144:145], v158
	ds_read_b64 v[146:147], v158 offset:8
	ds_read_b64 v[148:149], v158 offset:16
	s_waitcnt lgkmcnt(0)
	v_lshrrev_b32_e32 v1, 8, v166
	v_lshrrev_b32_e32 v52, 8, v167
	v_lshrrev_b32_e32 v53, 8, v241
	v_lshrrev_b32_e32 v158, 8, v161
	s_barrier
	v_mfma_scale_f32_16x16x128_f8f6f4 v[30:33], v[154:157], v[34:39], v[126:129], v240, v1 op_sel_hi:[0,0,0] cbsz:4 blgp:2
	v_mfma_scale_f32_16x16x128_f8f6f4 v[22:25], v[168:171], v[34:39], v[122:125], v240, v1 op_sel_hi:[0,0,0] cbsz:4 blgp:2
	v_mfma_scale_f32_16x16x128_f8f6f4 v[14:17], v[172:175], v[34:39], v[114:117], v240, v1 op_sel_hi:[0,0,0] cbsz:4 blgp:2
	v_mfma_scale_f32_16x16x128_f8f6f4 v[6:9], v[176:179], v[34:39], v[102:105], v240, v1 op_sel_hi:[0,0,0] cbsz:4 blgp:2
	v_mfma_scale_f32_16x16x128_f8f6f4 v[26:29], v[180:183], v[34:39], v[86:89], v240, v1 op_sel_hi:[0,0,0] cbsz:4 blgp:2
	v_mfma_scale_f32_16x16x128_f8f6f4 v[18:21], v[184:187], v[34:39], v[70:73], v240, v1 op_sel_hi:[0,0,0] cbsz:4 blgp:2
	v_mfma_scale_f32_16x16x128_f8f6f4 v[10:13], v[188:191], v[34:39], v[54:57], v240, v1 op_sel_hi:[0,0,0] cbsz:4 blgp:2
	v_mfma_scale_f32_16x16x128_f8f6f4 v[2:5], v[192:195], v[34:39], v[2:5], v240, v1 op_sel_hi:[0,0,0] cbsz:4 blgp:2
	v_mfma_scale_f32_16x16x128_f8f6f4 v[132:135], v[154:157], v[40:45], v[118:121], v240, v52 op_sel_hi:[0,0,0] cbsz:4 blgp:2
	v_mfma_scale_f32_16x16x128_f8f6f4 v[128:131], v[168:171], v[40:45], v[110:113], v240, v52 op_sel_hi:[0,0,0] cbsz:4 blgp:2
	v_mfma_scale_f32_16x16x128_f8f6f4 v[124:127], v[172:175], v[40:45], v[98:101], v240, v52 op_sel_hi:[0,0,0] cbsz:4 blgp:2
	v_mfma_scale_f32_16x16x128_f8f6f4 v[116:119], v[176:179], v[40:45], v[82:85], v240, v52 op_sel_hi:[0,0,0] cbsz:4 blgp:2
	v_mfma_scale_f32_16x16x128_f8f6f4 v[140:143], v[180:183], v[40:45], v[66:69], v240, v52 op_sel_hi:[0,0,0] cbsz:4 blgp:2
	v_mfma_scale_f32_16x16x128_f8f6f4 v[136:139], v[184:187], v[40:45], v[162:165], v240, v52 op_sel_hi:[0,0,0] cbsz:4 blgp:2
	v_mfma_scale_f32_16x16x128_f8f6f4 v[120:123], v[188:191], v[40:45], v[196:199], v240, v52 op_sel_hi:[0,0,0] cbsz:4 blgp:2
	v_mfma_scale_f32_16x16x128_f8f6f4 v[112:115], v[192:195], v[40:45], v[200:203], v240, v52 op_sel_hi:[0,0,0] cbsz:4 blgp:2
	v_mfma_scale_f32_16x16x128_f8f6f4 v[100:103], v[154:157], v[46:51], v[106:109], v240, v53 op_sel_hi:[0,0,0] cbsz:4 blgp:2
	v_mfma_scale_f32_16x16x128_f8f6f4 v[96:99], v[168:171], v[46:51], v[94:97], v240, v53 op_sel_hi:[0,0,0] cbsz:4 blgp:2
	v_mfma_scale_f32_16x16x128_f8f6f4 v[92:95], v[172:175], v[46:51], v[78:81], v240, v53 op_sel_hi:[0,0,0] cbsz:4 blgp:2
	v_mfma_scale_f32_16x16x128_f8f6f4 v[84:87], v[176:179], v[46:51], v[62:65], v240, v53 op_sel_hi:[0,0,0] cbsz:4 blgp:2
	v_mfma_scale_f32_16x16x128_f8f6f4 v[108:111], v[180:183], v[46:51], v[204:207], v240, v53 op_sel_hi:[0,0,0] cbsz:4 blgp:2
	v_mfma_scale_f32_16x16x128_f8f6f4 v[104:107], v[184:187], v[46:51], v[208:211], v240, v53 op_sel_hi:[0,0,0] cbsz:4 blgp:2
	v_mfma_scale_f32_16x16x128_f8f6f4 v[88:91], v[188:191], v[46:51], v[212:215], v240, v53 op_sel_hi:[0,0,0] cbsz:4 blgp:2
	v_mfma_scale_f32_16x16x128_f8f6f4 v[80:83], v[192:195], v[46:51], v[216:219], v240, v53 op_sel_hi:[0,0,0] cbsz:4 blgp:2
	v_mfma_scale_f32_16x16x128_f8f6f4 v[68:71], v[154:157], v[144:149], v[220:223], v240, v158 op_sel_hi:[0,0,0] cbsz:4 blgp:2
	v_mfma_scale_f32_16x16x128_f8f6f4 v[64:67], v[168:171], v[144:149], v[74:77], v240, v158 op_sel_hi:[0,0,0] cbsz:4 blgp:2
	v_mfma_scale_f32_16x16x128_f8f6f4 v[60:63], v[172:175], v[144:149], v[58:61], v240, v158 op_sel_hi:[0,0,0] cbsz:4 blgp:2
	v_mfma_scale_f32_16x16x128_f8f6f4 v[52:55], v[176:179], v[144:149], v[224:227], v240, v158 op_sel_hi:[0,0,0] cbsz:4 blgp:2
	v_mfma_scale_f32_16x16x128_f8f6f4 v[76:79], v[180:183], v[144:149], v[228:231], v240, v158 op_sel_hi:[0,0,0] cbsz:4 blgp:2
	v_mfma_scale_f32_16x16x128_f8f6f4 v[72:75], v[184:187], v[144:149], v[232:235], v240, v158 op_sel_hi:[0,0,0] cbsz:4 blgp:2
	v_mfma_scale_f32_16x16x128_f8f6f4 v[56:59], v[188:191], v[144:149], v[236:239], v240, v158 op_sel_hi:[0,0,0] cbsz:4 blgp:2
	v_mfma_scale_f32_16x16x128_f8f6f4 v[48:51], v[192:195], v[144:149], v[150:153], v240, v158 op_sel_hi:[0,0,0] cbsz:4 blgp:2
	s_barrier
	s_cmpk_gt_u32 s33, 0xff
	s_cbranch_scc1 .LBB2_6
	s_barrier

.LBB3_3:
	s_add_i32 s42, s60, 0xfffff000
	s_and_b32 s42, s42, 0x1000
	ds_read_b128 v[202:205], v175
	ds_read_b128 v[206:209], v175 offset:256
	ds_read_b128 v[210:213], v175 offset:512
	ds_read_b128 v[214:217], v175 offset:768
	ds_read_b128 v[218:221], v175 offset:1024
	ds_read_b128 v[222:225], v175 offset:1280
	ds_read_b128 v[226:229], v175 offset:1536
	ds_read_b128 v[230:233], v175 offset:1792
	ds_read2_b64 v[178:181], v171 offset1:1
	ds_read2_b64 v[182:185], v171 offset0:2 offset1:48
	ds_read2_b64 v[186:189], v171 offset0:49 offset1:50
	s_mov_b32 m0, s57
	ds_read2_b64 v[190:193], v171 offset0:96 offset1:97
	global_load_lds_dwordx4 v144, s[76:77]
	s_mov_b32 m0, s56
	ds_read2_b64 v[194:197], v171 offset0:98 offset1:144
	global_load_lds_dwordx4 v145, s[76:77]
	s_mov_b32 m0, s55
	ds_read2_b64 v[198:201], v171 offset0:145 offset1:146
	global_load_lds_dwordx4 v146, s[76:77]
	v_add_u32_e32 v152, s42, v176
	ds_read_u16 v240, v152
	ds_read_u16 v241, v152 offset:32
	ds_read_u16 v242, v152 offset:64
	s_add_i32 s42, s60, 0xfffff800
	s_and_b32 s42, s42, 0x1800
	s_add_i32 m0, s48, s42
	ds_read_u16 v243, v152 offset:96
	global_load_lds_dword v150, s[80:81]
	s_waitcnt vmcnt(6)
	s_waitcnt lgkmcnt(0)
	s_barrier
	v_mfma_scale_f32_16x16x128_f8f6f4 v[126:129], v[202:205], v[178:183], v[126:129], v177, v240 op_sel_hi:[0,0,0] cbsz:4 blgp:2
	v_mfma_scale_f32_16x16x128_f8f6f4 v[122:125], v[206:209], v[178:183], v[122:125], v177, v240 op_sel_hi:[0,0,0] cbsz:4 blgp:2
	v_mfma_scale_f32_16x16x128_f8f6f4 v[114:117], v[210:213], v[178:183], v[114:117], v177, v240 op_sel_hi:[0,0,0] cbsz:4 blgp:2
	v_mfma_scale_f32_16x16x128_f8f6f4 v[102:105], v[214:217], v[178:183], v[102:105], v177, v240 op_sel_hi:[0,0,0] cbsz:4 blgp:2
	v_mfma_scale_f32_16x16x128_f8f6f4 v[86:89], v[218:221], v[178:183], v[86:89], v177, v240 op_sel_hi:[0,0,0] cbsz:4 blgp:2
	v_mfma_scale_f32_16x16x128_f8f6f4 v[70:73], v[222:225], v[178:183], v[70:73], v177, v240 op_sel_hi:[0,0,0] cbsz:4 blgp:2
	v_mfma_scale_f32_16x16x128_f8f6f4 v[54:57], v[226:229], v[178:183], v[54:57], v177, v240 op_sel_hi:[0,0,0] cbsz:4 blgp:2
	v_mfma_scale_f32_16x16x128_f8f6f4 v[38:41], v[230:233], v[178:183], v[38:41], v177, v240 op_sel_hi:[0,0,0] cbsz:4 blgp:2
	v_mfma_scale_f32_16x16x128_f8f6f4 v[118:121], v[202:205], v[184:189], v[118:121], v177, v241 op_sel_hi:[0,0,0] cbsz:4 blgp:2
	v_mfma_scale_f32_16x16x128_f8f6f4 v[110:113], v[206:209], v[184:189], v[110:113], v177, v241 op_sel_hi:[0,0,0] cbsz:4 blgp:2
	v_mfma_scale_f32_16x16x128_f8f6f4 v[98:101], v[210:213], v[184:189], v[98:101], v177, v241 op_sel_hi:[0,0,0] cbsz:4 blgp:2
	v_mfma_scale_f32_16x16x128_f8f6f4 v[82:85], v[214:217], v[184:189], v[82:85], v177, v241 op_sel_hi:[0,0,0] cbsz:4 blgp:2
	v_mfma_scale_f32_16x16x128_f8f6f4 v[66:69], v[218:221], v[184:189], v[66:69], v177, v241 op_sel_hi:[0,0,0] cbsz:4 blgp:2
	v_mfma_scale_f32_16x16x128_f8f6f4 v[50:53], v[222:225], v[184:189], v[50:53], v177, v241 op_sel_hi:[0,0,0] cbsz:4 blgp:2
	v_mfma_scale_f32_16x16x128_f8f6f4 v[34:37], v[226:229], v[184:189], v[34:37], v177, v241 op_sel_hi:[0,0,0] cbsz:4 blgp:2
	v_mfma_scale_f32_16x16x128_f8f6f4 v[106:109], v[202:205], v[190:195], v[106:109], v177, v242 op_sel_hi:[0,0,0] cbsz:4 blgp:2
	v_mfma_scale_f32_16x16x128_f8f6f4 v[94:97], v[206:209], v[190:195], v[94:97], v177, v242 op_sel_hi:[0,0,0] cbsz:4 blgp:2
	v_mfma_scale_f32_16x16x128_f8f6f4 v[78:81], v[210:213], v[190:195], v[78:81], v177, v242 op_sel_hi:[0,0,0] cbsz:4 blgp:2
	v_mfma_scale_f32_16x16x128_f8f6f4 v[62:65], v[214:217], v[190:195], v[62:65], v177, v242 op_sel_hi:[0,0,0] cbsz:4 blgp:2
	v_mfma_scale_f32_16x16x128_f8f6f4 v[46:49], v[218:221], v[190:195], v[46:49], v177, v242 op_sel_hi:[0,0,0] cbsz:4 blgp:2
	v_mfma_scale_f32_16x16x128_f8f6f4 v[30:33], v[222:225], v[190:195], v[30:33], v177, v242 op_sel_hi:[0,0,0] cbsz:4 blgp:2
	v_mfma_scale_f32_16x16x128_f8f6f4 v[90:93], v[202:205], v[196:201], v[90:93], v177, v243 op_sel_hi:[0,0,0] cbsz:4 blgp:2
	v_mfma_scale_f32_16x16x128_f8f6f4 v[74:77], v[206:209], v[196:201], v[74:77], v177, v243 op_sel_hi:[0,0,0] cbsz:4 blgp:2
	v_mfma_scale_f32_16x16x128_f8f6f4 v[58:61], v[210:213], v[196:201], v[58:61], v177, v243 op_sel_hi:[0,0,0] cbsz:4 blgp:2
	v_mfma_scale_f32_16x16x128_f8f6f4 v[42:45], v[214:217], v[196:201], v[42:45], v177, v243 op_sel_hi:[0,0,0] cbsz:4 blgp:2
	v_mfma_scale_f32_16x16x128_f8f6f4 v[26:29], v[218:221], v[196:201], v[26:29], v177, v243 op_sel_hi:[0,0,0] cbsz:4 blgp:2
	v_mfma_scale_f32_16x16x128_f8f6f4 v[178:181], v[230:233], v[184:189], v[22:25], v177, v241 op_sel_hi:[0,0,0] cbsz:4 blgp:2
	v_mfma_scale_f32_16x16x128_f8f6f4 v[182:185], v[226:229], v[190:195], v[18:21], v177, v242 op_sel_hi:[0,0,0] cbsz:4 blgp:2
	v_mfma_scale_f32_16x16x128_f8f6f4 v[186:189], v[230:233], v[190:195], v[10:13], v177, v242 op_sel_hi:[0,0,0] cbsz:4 blgp:2
	v_mfma_scale_f32_16x16x128_f8f6f4 v[190:193], v[222:225], v[196:201], v[14:17], v177, v243 op_sel_hi:[0,0,0] cbsz:4 blgp:2
	v_mfma_scale_f32_16x16x128_f8f6f4 v[234:237], v[226:229], v[196:201], v[6:9], v177, v243 op_sel_hi:[0,0,0] cbsz:4 blgp:2
	v_mfma_scale_f32_16x16x128_f8f6f4 v[194:197], v[230:233], v[196:201], v[2:5], v177, v243 op_sel_hi:[0,0,0] cbsz:4 blgp:2
	s_barrier
	ds_read2_b64 v[2:5], v167 offset1:1
	s_mov_b32 m0, s52
	ds_read2_b64 v[6:9], v167 offset0:2 offset1:48
	global_load_lds_dwordx4 v147, s[76:77]
	s_mov_b32 m0, s50
	ds_read2_b64 v[10:13], v167 offset0:49 offset1:50
	global_load_lds_dwordx4 v148, s[76:77]
	s_mov_b32 m0, s49
	ds_read2_b64 v[14:17], v167 offset0:96 offset1:97
	global_load_lds_dwordx4 v149, s[76:77]
	s_mov_b32 m0, s13
	ds_read2_b64 v[18:21], v167 offset0:98 offset1:144
	global_load_lds_dwordx4 v142, s[72:73]
	s_mov_b32 m0, s44
	ds_read2_b64 v[22:25], v167 offset0:145 offset1:146
	global_load_lds_dwordx4 v143, s[72:73]
	s_waitcnt vmcnt(5)
	s_waitcnt lgkmcnt(0)
	s_barrier
	v_mfma_scale_f32_16x16x128_f8f6f4 v[126:129], v[202:205], v[2:7], v[126:129], v177, v240 op_sel:[0,1,0] op_sel_hi:[0,0,0] cbsz:4 blgp:2
	v_mfma_scale_f32_16x16x128_f8f6f4 v[122:125], v[206:209], v[2:7], v[122:125], v177, v240 op_sel:[0,1,0] op_sel_hi:[0,0,0] cbsz:4 blgp:2
	v_mfma_scale_f32_16x16x128_f8f6f4 v[114:117], v[210:213], v[2:7], v[114:117], v177, v240 op_sel:[0,1,0] op_sel_hi:[0,0,0] cbsz:4 blgp:2
	v_mfma_scale_f32_16x16x128_f8f6f4 v[102:105], v[214:217], v[2:7], v[102:105], v177, v240 op_sel:[0,1,0] op_sel_hi:[0,0,0] cbsz:4 blgp:2
	v_mfma_scale_f32_16x16x128_f8f6f4 v[86:89], v[218:221], v[2:7], v[86:89], v177, v240 op_sel:[0,1,0] op_sel_hi:[0,0,0] cbsz:4 blgp:2
	v_mfma_scale_f32_16x16x128_f8f6f4 v[70:73], v[222:225], v[2:7], v[70:73], v177, v240 op_sel:[0,1,0] op_sel_hi:[0,0,0] cbsz:4 blgp:2
	v_mfma_scale_f32_16x16x128_f8f6f4 v[54:57], v[226:229], v[2:7], v[54:57], v177, v240 op_sel:[0,1,0] op_sel_hi:[0,0,0] cbsz:4 blgp:2
	v_mfma_scale_f32_16x16x128_f8f6f4 v[38:41], v[230:233], v[2:7], v[38:41], v177, v240 op_sel:[0,1,0] op_sel_hi:[0,0,0] cbsz:4 blgp:2
	v_mfma_scale_f32_16x16x128_f8f6f4 v[118:121], v[202:205], v[8:13], v[118:121], v177, v241 op_sel:[0,1,0] op_sel_hi:[0,0,0] cbsz:4 blgp:2
	v_mfma_scale_f32_16x16x128_f8f6f4 v[110:113], v[206:209], v[8:13], v[110:113], v177, v241 op_sel:[0,1,0] op_sel_hi:[0,0,0] cbsz:4 blgp:2
	v_mfma_scale_f32_16x16x128_f8f6f4 v[98:101], v[210:213], v[8:13], v[98:101], v177, v241 op_sel:[0,1,0] op_sel_hi:[0,0,0] cbsz:4 blgp:2
	v_mfma_scale_f32_16x16x128_f8f6f4 v[82:85], v[214:217], v[8:13], v[82:85], v177, v241 op_sel:[0,1,0] op_sel_hi:[0,0,0] cbsz:4 blgp:2
	v_mfma_scale_f32_16x16x128_f8f6f4 v[66:69], v[218:221], v[8:13], v[66:69], v177, v241 op_sel:[0,1,0] op_sel_hi:[0,0,0] cbsz:4 blgp:2
	v_mfma_scale_f32_16x16x128_f8f6f4 v[50:53], v[222:225], v[8:13], v[50:53], v177, v241 op_sel:[0,1,0] op_sel_hi:[0,0,0] cbsz:4 blgp:2
	v_mfma_scale_f32_16x16x128_f8f6f4 v[34:37], v[226:229], v[8:13], v[34:37], v177, v241 op_sel:[0,1,0] op_sel_hi:[0,0,0] cbsz:4 blgp:2
	v_mfma_scale_f32_16x16x128_f8f6f4 v[106:109], v[202:205], v[14:19], v[106:109], v177, v242 op_sel:[0,1,0] op_sel_hi:[0,0,0] cbsz:4 blgp:2
	v_mfma_scale_f32_16x16x128_f8f6f4 v[94:97], v[206:209], v[14:19], v[94:97], v177, v242 op_sel:[0,1,0] op_sel_hi:[0,0,0] cbsz:4 blgp:2
	v_mfma_scale_f32_16x16x128_f8f6f4 v[78:81], v[210:213], v[14:19], v[78:81], v177, v242 op_sel:[0,1,0] op_sel_hi:[0,0,0] cbsz:4 blgp:2
	v_mfma_scale_f32_16x16x128_f8f6f4 v[62:65], v[214:217], v[14:19], v[62:65], v177, v242 op_sel:[0,1,0] op_sel_hi:[0,0,0] cbsz:4 blgp:2
	v_mfma_scale_f32_16x16x128_f8f6f4 v[46:49], v[218:221], v[14:19], v[46:49], v177, v242 op_sel:[0,1,0] op_sel_hi:[0,0,0] cbsz:4 blgp:2
	v_mfma_scale_f32_16x16x128_f8f6f4 v[30:33], v[222:225], v[14:19], v[30:33], v177, v242 op_sel:[0,1,0] op_sel_hi:[0,0,0] cbsz:4 blgp:2
	v_mfma_scale_f32_16x16x128_f8f6f4 v[90:93], v[202:205], v[20:25], v[90:93], v177, v243 op_sel:[0,1,0] op_sel_hi:[0,0,0] cbsz:4 blgp:2
	v_mfma_scale_f32_16x16x128_f8f6f4 v[74:77], v[206:209], v[20:25], v[74:77], v177, v243 op_sel:[0,1,0] op_sel_hi:[0,0,0] cbsz:4 blgp:2
	v_mfma_scale_f32_16x16x128_f8f6f4 v[58:61], v[210:213], v[20:25], v[58:61], v177, v243 op_sel:[0,1,0] op_sel_hi:[0,0,0] cbsz:4 blgp:2
	v_mfma_scale_f32_16x16x128_f8f6f4 v[42:45], v[214:217], v[20:25], v[42:45], v177, v243 op_sel:[0,1,0] op_sel_hi:[0,0,0] cbsz:4 blgp:2
	v_mfma_scale_f32_16x16x128_f8f6f4 v[26:29], v[218:221], v[20:25], v[26:29], v177, v243 op_sel:[0,1,0] op_sel_hi:[0,0,0] cbsz:4 blgp:2
	v_mfma_scale_f32_16x16x128_f8f6f4 v[178:181], v[230:233], v[8:13], v[178:181], v177, v241 op_sel:[0,1,0] op_sel_hi:[0,0,0] cbsz:4 blgp:2
	v_mfma_scale_f32_16x16x128_f8f6f4 v[182:185], v[226:229], v[14:19], v[182:185], v177, v242 op_sel:[0,1,0] op_sel_hi:[0,0,0] cbsz:4 blgp:2
	v_mfma_scale_f32_16x16x128_f8f6f4 v[186:189], v[230:233], v[14:19], v[186:189], v177, v242 op_sel:[0,1,0] op_sel_hi:[0,0,0] cbsz:4 blgp:2
	v_mfma_scale_f32_16x16x128_f8f6f4 v[190:193], v[222:225], v[20:25], v[190:193], v177, v243 op_sel:[0,1,0] op_sel_hi:[0,0,0] cbsz:4 blgp:2
	v_mfma_scale_f32_16x16x128_f8f6f4 v[198:201], v[226:229], v[20:25], v[234:237], v177, v243 op_sel:[0,1,0] op_sel_hi:[0,0,0] cbsz:4 blgp:2
	v_mfma_scale_f32_16x16x128_f8f6f4 v[194:197], v[230:233], v[20:25], v[194:197], v177, v243 op_sel:[0,1,0] op_sel_hi:[0,0,0] cbsz:4 blgp:2
	s_barrier
	ds_read_b128 v[202:205], v166
	ds_read_b128 v[206:209], v166 offset:256
	ds_read_b128 v[210:213], v166 offset:512
	ds_read_b128 v[214:217], v166 offset:768
	ds_read_b128 v[218:221], v166 offset:1024
	ds_read_b128 v[222:225], v166 offset:1280
	ds_read_b128 v[226:229], v166 offset:1536
	ds_read_b128 v[230:233], v166 offset:1792
	ds_read2_b64 v[2:5], v162 offset1:1
	ds_read2_b64 v[6:9], v162 offset0:2 offset1:48
	ds_read2_b64 v[10:13], v162 offset0:49 offset1:50
	s_mov_b32 m0, s45
	ds_read2_b64 v[14:17], v162 offset0:96 offset1:97
	global_load_lds_dwordx4 v144, s[78:79]
	s_mov_b32 m0, s46
	ds_read2_b64 v[18:21], v162 offset0:98 offset1:144
	global_load_lds_dwordx4 v145, s[78:79]
	s_mov_b32 m0, s47
	ds_read2_b64 v[22:25], v162 offset0:145 offset1:146
	global_load_lds_dwordx4 v146, s[78:79]
	v_add_u32_e32 v234, s42, v176
	ds_read_u16 v242, v234
	ds_read_u16 v243, v234 offset:32
	ds_read_u16 v244, v234 offset:64
	s_and_b32 s42, s60, 0x1000
	s_add_i32 m0, s48, s42
	ds_read_u16 v245, v234 offset:96
	global_load_lds_dword v151, s[80:81]
	s_waitcnt vmcnt(6)
	s_waitcnt lgkmcnt(0)
	s_barrier
	v_mfma_scale_f32_16x16x128_f8f6f4 v[126:129], v[202:205], v[2:7], v[126:129], v177, v242 op_sel_hi:[0,0,0] cbsz:4 blgp:2
	v_mfma_scale_f32_16x16x128_f8f6f4 v[122:125], v[206:209], v[2:7], v[122:125], v177, v242 op_sel_hi:[0,0,0] cbsz:4 blgp:2
	v_mfma_scale_f32_16x16x128_f8f6f4 v[114:117], v[210:213], v[2:7], v[114:117], v177, v242 op_sel_hi:[0,0,0] cbsz:4 blgp:2
	v_mfma_scale_f32_16x16x128_f8f6f4 v[102:105], v[214:217], v[2:7], v[102:105], v177, v242 op_sel_hi:[0,0,0] cbsz:4 blgp:2
	v_mfma_scale_f32_16x16x128_f8f6f4 v[86:89], v[218:221], v[2:7], v[86:89], v177, v242 op_sel_hi:[0,0,0] cbsz:4 blgp:2
	v_mfma_scale_f32_16x16x128_f8f6f4 v[70:73], v[222:225], v[2:7], v[70:73], v177, v242 op_sel_hi:[0,0,0] cbsz:4 blgp:2
	v_mfma_scale_f32_16x16x128_f8f6f4 v[54:57], v[226:229], v[2:7], v[54:57], v177, v242 op_sel_hi:[0,0,0] cbsz:4 blgp:2
	v_mfma_scale_f32_16x16x128_f8f6f4 v[38:41], v[230:233], v[2:7], v[38:41], v177, v242 op_sel_hi:[0,0,0] cbsz:4 blgp:2
	v_mfma_scale_f32_16x16x128_f8f6f4 v[118:121], v[202:205], v[8:13], v[118:121], v177, v243 op_sel_hi:[0,0,0] cbsz:4 blgp:2
	v_mfma_scale_f32_16x16x128_f8f6f4 v[110:113], v[206:209], v[8:13], v[110:113], v177, v243 op_sel_hi:[0,0,0] cbsz:4 blgp:2
	v_mfma_scale_f32_16x16x128_f8f6f4 v[98:101], v[210:213], v[8:13], v[98:101], v177, v243 op_sel_hi:[0,0,0] cbsz:4 blgp:2
	v_mfma_scale_f32_16x16x128_f8f6f4 v[82:85], v[214:217], v[8:13], v[82:85], v177, v243 op_sel_hi:[0,0,0] cbsz:4 blgp:2
	v_mfma_scale_f32_16x16x128_f8f6f4 v[66:69], v[218:221], v[8:13], v[66:69], v177, v243 op_sel_hi:[0,0,0] cbsz:4 blgp:2
	v_mfma_scale_f32_16x16x128_f8f6f4 v[50:53], v[222:225], v[8:13], v[50:53], v177, v243 op_sel_hi:[0,0,0] cbsz:4 blgp:2
	v_mfma_scale_f32_16x16x128_f8f6f4 v[34:37], v[226:229], v[8:13], v[34:37], v177, v243 op_sel_hi:[0,0,0] cbsz:4 blgp:2
	v_mfma_scale_f32_16x16x128_f8f6f4 v[106:109], v[202:205], v[14:19], v[106:109], v177, v244 op_sel_hi:[0,0,0] cbsz:4 blgp:2
	v_mfma_scale_f32_16x16x128_f8f6f4 v[94:97], v[206:209], v[14:19], v[94:97], v177, v244 op_sel_hi:[0,0,0] cbsz:4 blgp:2
	v_mfma_scale_f32_16x16x128_f8f6f4 v[78:81], v[210:213], v[14:19], v[78:81], v177, v244 op_sel_hi:[0,0,0] cbsz:4 blgp:2
	v_mfma_scale_f32_16x16x128_f8f6f4 v[62:65], v[214:217], v[14:19], v[62:65], v177, v244 op_sel_hi:[0,0,0] cbsz:4 blgp:2
	v_mfma_scale_f32_16x16x128_f8f6f4 v[46:49], v[218:221], v[14:19], v[46:49], v177, v244 op_sel_hi:[0,0,0] cbsz:4 blgp:2
	v_mfma_scale_f32_16x16x128_f8f6f4 v[30:33], v[222:225], v[14:19], v[30:33], v177, v244 op_sel_hi:[0,0,0] cbsz:4 blgp:2
	v_mfma_scale_f32_16x16x128_f8f6f4 v[238:241], v[226:229], v[14:19], v[182:185], v177, v244 op_sel_hi:[0,0,0] cbsz:4 blgp:2
	v_mfma_scale_f32_16x16x128_f8f6f4 v[14:17], v[230:233], v[14:19], v[186:189], v177, v244 op_sel_hi:[0,0,0] cbsz:4 blgp:2
	v_mfma_scale_f32_16x16x128_f8f6f4 v[90:93], v[202:205], v[20:25], v[90:93], v177, v245 op_sel_hi:[0,0,0] cbsz:4 blgp:2
	v_mfma_scale_f32_16x16x128_f8f6f4 v[74:77], v[206:209], v[20:25], v[74:77], v177, v245 op_sel_hi:[0,0,0] cbsz:4 blgp:2
	v_mfma_scale_f32_16x16x128_f8f6f4 v[58:61], v[210:213], v[20:25], v[58:61], v177, v245 op_sel_hi:[0,0,0] cbsz:4 blgp:2
	v_mfma_scale_f32_16x16x128_f8f6f4 v[42:45], v[214:217], v[20:25], v[42:45], v177, v245 op_sel_hi:[0,0,0] cbsz:4 blgp:2
	v_mfma_scale_f32_16x16x128_f8f6f4 v[26:29], v[218:221], v[20:25], v[26:29], v177, v245 op_sel_hi:[0,0,0] cbsz:4 blgp:2
	v_mfma_scale_f32_16x16x128_f8f6f4 v[234:237], v[230:233], v[8:13], v[178:181], v177, v243 op_sel_hi:[0,0,0] cbsz:4 blgp:2
	v_mfma_scale_f32_16x16x128_f8f6f4 v[190:193], v[222:225], v[20:25], v[190:193], v177, v245 op_sel_hi:[0,0,0] cbsz:4 blgp:2
	v_mfma_scale_f32_16x16x128_f8f6f4 v[198:201], v[226:229], v[20:25], v[198:201], v177, v245 op_sel_hi:[0,0,0] cbsz:4 blgp:2
	v_mfma_scale_f32_16x16x128_f8f6f4 v[194:197], v[230:233], v[20:25], v[194:197], v177, v245 op_sel_hi:[0,0,0] cbsz:4 blgp:2
	s_barrier
	ds_read2_b64 v[2:5], v1 offset1:1
	s_mov_b32 m0, s51
	ds_read2_b64 v[6:9], v1 offset0:2 offset1:48
	global_load_lds_dwordx4 v147, s[78:79]
	s_mov_b32 m0, s53
	ds_read2_b64 v[10:13], v1 offset0:49 offset1:50
	global_load_lds_dwordx4 v148, s[78:79]
	s_mov_b32 m0, s54
	ds_read2_b64 v[178:181], v159 offset1:1
	global_load_lds_dwordx4 v149, s[78:79]
	s_mov_b32 m0, s61
	ds_read2_b64 v[182:185], v159 offset0:2 offset1:48
	global_load_lds_dwordx4 v142, s[74:75]
	s_mov_b32 m0, s58
	ds_read2_b64 v[186:189], v159 offset0:49 offset1:50
	global_load_lds_dwordx4 v143, s[74:75]
	s_waitcnt vmcnt(5)
	s_waitcnt lgkmcnt(0)
	s_barrier
	v_mfma_scale_f32_16x16x128_f8f6f4 v[126:129], v[202:205], v[2:7], v[126:129], v177, v242 op_sel:[0,1,0] op_sel_hi:[0,0,0] cbsz:4 blgp:2
	v_mfma_scale_f32_16x16x128_f8f6f4 v[122:125], v[206:209], v[2:7], v[122:125], v177, v242 op_sel:[0,1,0] op_sel_hi:[0,0,0] cbsz:4 blgp:2
	v_mfma_scale_f32_16x16x128_f8f6f4 v[114:117], v[210:213], v[2:7], v[114:117], v177, v242 op_sel:[0,1,0] op_sel_hi:[0,0,0] cbsz:4 blgp:2
	v_mfma_scale_f32_16x16x128_f8f6f4 v[102:105], v[214:217], v[2:7], v[102:105], v177, v242 op_sel:[0,1,0] op_sel_hi:[0,0,0] cbsz:4 blgp:2
	v_mfma_scale_f32_16x16x128_f8f6f4 v[86:89], v[218:221], v[2:7], v[86:89], v177, v242 op_sel:[0,1,0] op_sel_hi:[0,0,0] cbsz:4 blgp:2
	v_mfma_scale_f32_16x16x128_f8f6f4 v[70:73], v[222:225], v[2:7], v[70:73], v177, v242 op_sel:[0,1,0] op_sel_hi:[0,0,0] cbsz:4 blgp:2
	v_mfma_scale_f32_16x16x128_f8f6f4 v[54:57], v[226:229], v[2:7], v[54:57], v177, v242 op_sel:[0,1,0] op_sel_hi:[0,0,0] cbsz:4 blgp:2
	v_mfma_scale_f32_16x16x128_f8f6f4 v[38:41], v[230:233], v[2:7], v[38:41], v177, v242 op_sel:[0,1,0] op_sel_hi:[0,0,0] cbsz:4 blgp:2
	v_mfma_scale_f32_16x16x128_f8f6f4 v[118:121], v[202:205], v[8:13], v[118:121], v177, v243 op_sel:[0,1,0] op_sel_hi:[0,0,0] cbsz:4 blgp:2
	v_mfma_scale_f32_16x16x128_f8f6f4 v[110:113], v[206:209], v[8:13], v[110:113], v177, v243 op_sel:[0,1,0] op_sel_hi:[0,0,0] cbsz:4 blgp:2
	v_mfma_scale_f32_16x16x128_f8f6f4 v[98:101], v[210:213], v[8:13], v[98:101], v177, v243 op_sel:[0,1,0] op_sel_hi:[0,0,0] cbsz:4 blgp:2
	v_mfma_scale_f32_16x16x128_f8f6f4 v[82:85], v[214:217], v[8:13], v[82:85], v177, v243 op_sel:[0,1,0] op_sel_hi:[0,0,0] cbsz:4 blgp:2
	v_mfma_scale_f32_16x16x128_f8f6f4 v[66:69], v[218:221], v[8:13], v[66:69], v177, v243 op_sel:[0,1,0] op_sel_hi:[0,0,0] cbsz:4 blgp:2
	v_mfma_scale_f32_16x16x128_f8f6f4 v[50:53], v[222:225], v[8:13], v[50:53], v177, v243 op_sel:[0,1,0] op_sel_hi:[0,0,0] cbsz:4 blgp:2
	v_mfma_scale_f32_16x16x128_f8f6f4 v[34:37], v[226:229], v[8:13], v[34:37], v177, v243 op_sel:[0,1,0] op_sel_hi:[0,0,0] cbsz:4 blgp:2
	v_mfma_scale_f32_16x16x128_f8f6f4 v[22:25], v[230:233], v[8:13], v[234:237], v177, v243 op_sel:[0,1,0] op_sel_hi:[0,0,0] cbsz:4 blgp:2
	v_mfma_scale_f32_16x16x128_f8f6f4 v[106:109], v[202:205], v[178:183], v[106:109], v177, v244 op_sel:[0,1,0] op_sel_hi:[0,0,0] cbsz:4 blgp:2
	v_mfma_scale_f32_16x16x128_f8f6f4 v[94:97], v[206:209], v[178:183], v[94:97], v177, v244 op_sel:[0,1,0] op_sel_hi:[0,0,0] cbsz:4 blgp:2
	v_mfma_scale_f32_16x16x128_f8f6f4 v[78:81], v[210:213], v[178:183], v[78:81], v177, v244 op_sel:[0,1,0] op_sel_hi:[0,0,0] cbsz:4 blgp:2
	v_mfma_scale_f32_16x16x128_f8f6f4 v[62:65], v[214:217], v[178:183], v[62:65], v177, v244 op_sel:[0,1,0] op_sel_hi:[0,0,0] cbsz:4 blgp:2
	v_mfma_scale_f32_16x16x128_f8f6f4 v[46:49], v[218:221], v[178:183], v[46:49], v177, v244 op_sel:[0,1,0] op_sel_hi:[0,0,0] cbsz:4 blgp:2
	v_mfma_scale_f32_16x16x128_f8f6f4 v[30:33], v[222:225], v[178:183], v[30:33], v177, v244 op_sel:[0,1,0] op_sel_hi:[0,0,0] cbsz:4 blgp:2
	v_mfma_scale_f32_16x16x128_f8f6f4 v[18:21], v[226:229], v[178:183], v[238:241], v177, v244 op_sel:[0,1,0] op_sel_hi:[0,0,0] cbsz:4 blgp:2
	v_mfma_scale_f32_16x16x128_f8f6f4 v[10:13], v[230:233], v[178:183], v[14:17], v177, v244 op_sel:[0,1,0] op_sel_hi:[0,0,0] cbsz:4 blgp:2
	v_mfma_scale_f32_16x16x128_f8f6f4 v[90:93], v[202:205], v[184:189], v[90:93], v177, v245 op_sel:[0,1,0] op_sel_hi:[0,0,0] cbsz:4 blgp:2
	v_mfma_scale_f32_16x16x128_f8f6f4 v[74:77], v[206:209], v[184:189], v[74:77], v177, v245 op_sel:[0,1,0] op_sel_hi:[0,0,0] cbsz:4 blgp:2
	v_mfma_scale_f32_16x16x128_f8f6f4 v[58:61], v[210:213], v[184:189], v[58:61], v177, v245 op_sel:[0,1,0] op_sel_hi:[0,0,0] cbsz:4 blgp:2
	v_mfma_scale_f32_16x16x128_f8f6f4 v[42:45], v[214:217], v[184:189], v[42:45], v177, v245 op_sel:[0,1,0] op_sel_hi:[0,0,0] cbsz:4 blgp:2
	v_mfma_scale_f32_16x16x128_f8f6f4 v[26:29], v[218:221], v[184:189], v[26:29], v177, v245 op_sel:[0,1,0] op_sel_hi:[0,0,0] cbsz:4 blgp:2
	v_mfma_scale_f32_16x16x128_f8f6f4 v[14:17], v[222:225], v[184:189], v[190:193], v177, v245 op_sel:[0,1,0] op_sel_hi:[0,0,0] cbsz:4 blgp:2
	v_mfma_scale_f32_16x16x128_f8f6f4 v[6:9], v[226:229], v[184:189], v[198:201], v177, v245 op_sel:[0,1,0] op_sel_hi:[0,0,0] cbsz:4 blgp:2
	v_mfma_scale_f32_16x16x128_f8f6f4 v[2:5], v[230:233], v[184:189], v[194:197], v177, v245 op_sel:[0,1,0] op_sel_hi:[0,0,0] cbsz:4 blgp:2
	s_barrier
	s_add_i32 s59, s59, 2
	s_addk_i32 s60, 0x1000
	s_add_u32 s72, s72, 0x8000
	s_addc_u32 s73, s73, 0
	s_add_u32 s74, s74, 0x8000
	s_addc_u32 s75, s75, 0
	s_add_u32 s76, s76, 0x18000
	s_addc_u32 s77, s77, 0
	s_add_u32 s78, s78, 0x18000
	s_addc_u32 s79, s79, 0
	s_add_u32 s80, s80, 0x1000
	s_addc_u32 s81, s81, 0
	s_cmp_lt_u32 s59, 28
	s_cbranch_scc1 .LBB3_3
	ds_read_b128 v[154:157], v175
	ds_read_b128 v[186:189], v175 offset:256
	ds_read_b128 v[190:193], v175 offset:512
	ds_read_b128 v[194:197], v175 offset:768
	ds_read_b128 v[198:201], v175 offset:1024
	ds_read_b128 v[202:205], v175 offset:1280
	ds_read_b128 v[206:209], v175 offset:1536
	ds_read_b128 v[210:213], v175 offset:1792
	ds_read_b64 v[142:143], v171
	ds_read_b64 v[144:145], v171 offset:8
	ds_read_b64 v[146:147], v171 offset:16
	ds_read_b64 v[148:149], v174
	ds_read_b64 v[150:151], v174 offset:8
	ds_read_b64 v[152:153], v174 offset:16
	ds_read_b64 v[174:175], v173
	ds_read_b64 v[176:177], v173 offset:8
	ds_read_b64 v[178:179], v173 offset:16
	ds_read_b64 v[180:181], v172
	ds_read_b64 v[182:183], v172 offset:8
	ds_read_b64 v[184:185], v172 offset:16
	v_add_u32_e32 v171, 0x21000, v248
	v_add_u32_e32 v172, 0x21020, v248
	v_add_u32_e32 v173, 0x21040, v248
	v_add_u32_e32 v214, 0x21060, v248
	s_mov_b64 s[0:1], 0x7c000
	s_mov_b32 m0, s61
	ds_read_u16 v171, v171
	ds_read_u16 v215, v172
	ds_read_u16 v216, v173
	ds_read_u16 v214, v214
	v_lshl_add_u64 v[172:173], v[138:139], 0, s[0:1]
	s_mov_b64 s[0:1], 0x7e000
	v_lshl_add_u64 v[138:139], v[138:139], 0, s[0:1]
	s_mov_b32 m0, s58
	s_mov_b64 s[0:1], 0x174000
	v_lshl_add_u64 v[138:139], v[140:141], 0, s[0:1]
	v_lshl_add_u64 v[140:141], v[138:139], 0, s[16:17]
	s_mov_b32 m0, s57
	v_lshl_add_u64 v[130:131], s[14:15], 0, v[130:131]
	global_load_lds_dwordx4 v[140:141], off
	v_lshl_add_u64 v[140:141], v[138:139], 0, s[18:19]
	s_mov_b32 m0, s56
	v_lshl_add_u64 v[138:139], v[138:139], 0, s[20:21]
	global_load_lds_dwordx4 v[140:141], off
	s_mov_b32 m0, s55
	s_mov_b64 s[0:1], 0xf800
	global_load_lds_dwordx4 v[138:139], off
	v_lshl_add_u64 v[130:131], v[130:131], 0, s[0:1]
	s_add_i32 m0, s9, 0x21800
	s_waitcnt lgkmcnt(0)
	v_mov_b32_e32 v172, v216
	global_load_lds_dword v[130:131], off
	s_waitcnt vmcnt(6)
	s_waitcnt lgkmcnt(0)
	v_mov_b32_e32 v130, v171
	v_mov_b32_e32 v131, v215
	v_mov_b32_e32 v217, v214
	s_barrier
	v_mov_b32_e32 v161, 0x7f7f7f7f
	s_nop 1
	v_mfma_scale_f32_16x16x128_f8f6f4 v[126:129], v[154:157], v[142:147], v[126:129], v161, v130 op_sel_hi:[0,0,0] cbsz:4 blgp:2
	v_mfma_scale_f32_16x16x128_f8f6f4 v[122:125], v[186:189], v[142:147], v[122:125], v161, v130 op_sel_hi:[0,0,0] cbsz:4 blgp:2
	v_mfma_scale_f32_16x16x128_f8f6f4 v[114:117], v[190:193], v[142:147], v[114:117], v161, v130 op_sel_hi:[0,0,0] cbsz:4 blgp:2
	v_mfma_scale_f32_16x16x128_f8f6f4 v[102:105], v[194:197], v[142:147], v[102:105], v161, v130 op_sel_hi:[0,0,0] cbsz:4 blgp:2
	v_mfma_scale_f32_16x16x128_f8f6f4 v[86:89], v[198:201], v[142:147], v[86:89], v161, v130 op_sel_hi:[0,0,0] cbsz:4 blgp:2
	v_mfma_scale_f32_16x16x128_f8f6f4 v[70:73], v[202:205], v[142:147], v[70:73], v161, v130 op_sel_hi:[0,0,0] cbsz:4 blgp:2
	v_mfma_scale_f32_16x16x128_f8f6f4 v[54:57], v[206:209], v[142:147], v[54:57], v161, v130 op_sel_hi:[0,0,0] cbsz:4 blgp:2
	v_mfma_scale_f32_16x16x128_f8f6f4 v[38:41], v[210:213], v[142:147], v[38:41], v161, v130 op_sel_hi:[0,0,0] cbsz:4 blgp:2
	v_mfma_scale_f32_16x16x128_f8f6f4 v[118:121], v[154:157], v[148:153], v[118:121], v161, v131 op_sel_hi:[0,0,0] cbsz:4 blgp:2
	v_mfma_scale_f32_16x16x128_f8f6f4 v[110:113], v[186:189], v[148:153], v[110:113], v161, v131 op_sel_hi:[0,0,0] cbsz:4 blgp:2
	v_mfma_scale_f32_16x16x128_f8f6f4 v[98:101], v[190:193], v[148:153], v[98:101], v161, v131 op_sel_hi:[0,0,0] cbsz:4 blgp:2
	v_mfma_scale_f32_16x16x128_f8f6f4 v[82:85], v[194:197], v[148:153], v[82:85], v161, v131 op_sel_hi:[0,0,0] cbsz:4 blgp:2
	v_mfma_scale_f32_16x16x128_f8f6f4 v[66:69], v[198:201], v[148:153], v[66:69], v161, v131 op_sel_hi:[0,0,0] cbsz:4 blgp:2
	v_mfma_scale_f32_16x16x128_f8f6f4 v[50:53], v[202:205], v[148:153], v[50:53], v161, v131 op_sel_hi:[0,0,0] cbsz:4 blgp:2
	v_mfma_scale_f32_16x16x128_f8f6f4 v[34:37], v[206:209], v[148:153], v[34:37], v161, v131 op_sel_hi:[0,0,0] cbsz:4 blgp:2
	v_mfma_scale_f32_16x16x128_f8f6f4 v[138:141], v[210:213], v[148:153], v[22:25], v161, v131 op_sel_hi:[0,0,0] cbsz:4 blgp:2
	v_mfma_scale_f32_16x16x128_f8f6f4 v[106:109], v[154:157], v[174:179], v[106:109], v161, v172 op_sel_hi:[0,0,0] cbsz:4 blgp:2
	v_mfma_scale_f32_16x16x128_f8f6f4 v[94:97], v[186:189], v[174:179], v[94:97], v161, v172 op_sel_hi:[0,0,0] cbsz:4 blgp:2
	v_mfma_scale_f32_16x16x128_f8f6f4 v[78:81], v[190:193], v[174:179], v[78:81], v161, v172 op_sel_hi:[0,0,0] cbsz:4 blgp:2
	v_mfma_scale_f32_16x16x128_f8f6f4 v[62:65], v[194:197], v[174:179], v[62:65], v161, v172 op_sel_hi:[0,0,0] cbsz:4 blgp:2
	v_mfma_scale_f32_16x16x128_f8f6f4 v[46:49], v[198:201], v[174:179], v[46:49], v161, v172 op_sel_hi:[0,0,0] cbsz:4 blgp:2
	v_mfma_scale_f32_16x16x128_f8f6f4 v[142:145], v[206:209], v[174:179], v[18:21], v161, v172 op_sel_hi:[0,0,0] cbsz:4 blgp:2
	v_mfma_scale_f32_16x16x128_f8f6f4 v[146:149], v[210:213], v[174:179], v[10:13], v161, v172 op_sel_hi:[0,0,0] cbsz:4 blgp:2
	v_mfma_scale_f32_16x16x128_f8f6f4 v[90:93], v[154:157], v[180:185], v[90:93], v161, v217 op_sel_hi:[0,0,0] cbsz:4 blgp:2
	v_mfma_scale_f32_16x16x128_f8f6f4 v[74:77], v[186:189], v[180:185], v[74:77], v161, v217 op_sel_hi:[0,0,0] cbsz:4 blgp:2
	v_mfma_scale_f32_16x16x128_f8f6f4 v[58:61], v[190:193], v[180:185], v[58:61], v161, v217 op_sel_hi:[0,0,0] cbsz:4 blgp:2
	v_mfma_scale_f32_16x16x128_f8f6f4 v[150:153], v[202:205], v[180:185], v[14:17], v161, v217 op_sel_hi:[0,0,0] cbsz:4 blgp:2
	v_mfma_scale_f32_16x16x128_f8f6f4 v[30:33], v[202:205], v[174:179], v[30:33], v161, v172 op_sel_hi:[0,0,0] cbsz:4 blgp:2
	v_mfma_scale_f32_16x16x128_f8f6f4 v[42:45], v[194:197], v[180:185], v[42:45], v161, v217 op_sel_hi:[0,0,0] cbsz:4 blgp:2
	v_mfma_scale_f32_16x16x128_f8f6f4 v[26:29], v[198:201], v[180:185], v[26:29], v161, v217 op_sel_hi:[0,0,0] cbsz:4 blgp:2
	v_mfma_scale_f32_16x16x128_f8f6f4 v[172:175], v[206:209], v[180:185], v[6:9], v161, v217 op_sel_hi:[0,0,0] cbsz:4 blgp:2
	v_mfma_scale_f32_16x16x128_f8f6f4 v[176:179], v[210:213], v[180:185], v[2:5], v161, v217 op_sel_hi:[0,0,0] cbsz:4 blgp:2
	s_barrier
	ds_read_b64 v[2:3], v167
	ds_read_b64 v[4:5], v167 offset:8
	ds_read_b64 v[6:7], v167 offset:16
	ds_read_b64 v[8:9], v170
	ds_read_b64 v[10:11], v170 offset:8
	ds_read_b64 v[12:13], v170 offset:16
	ds_read_b64 v[14:15], v169
	ds_read_b64 v[16:17], v169 offset:8
	ds_read_b64 v[18:19], v169 offset:16
	s_mov_b64 s[0:1], 0x175800
	s_mov_b32 m0, s52
	ds_read_b64 v[20:21], v168
	ds_read_b64 v[22:23], v168 offset:8
	ds_read_b64 v[24:25], v168 offset:16
	v_lshl_add_u64 v[130:131], v[132:133], 0, s[0:1]
	global_load_lds_dwordx4 v[130:131], off
	v_lshl_add_u64 v[130:131], v[134:135], 0, s[0:1]
	s_mov_b32 m0, s50
	v_lshrrev_b32_e32 v167, 8, v216
	global_load_lds_dwordx4 v[130:131], off
	v_lshl_add_u64 v[130:131], v[136:137], 0, s[0:1]
	s_mov_b32 m0, s49
	v_lshrrev_b32_e32 v168, 8, v214
	global_load_lds_dwordx4 v[130:131], off
	s_waitcnt vmcnt(3)
	s_waitcnt lgkmcnt(0)
	v_lshrrev_b32_e32 v130, 8, v171
	v_lshrrev_b32_e32 v131, 8, v215
	s_barrier
	v_mfma_scale_f32_16x16x128_f8f6f4 v[126:129], v[154:157], v[2:7], v[126:129], v161, v130 op_sel_hi:[0,0,0] cbsz:4 blgp:2
	v_mfma_scale_f32_16x16x128_f8f6f4 v[122:125], v[186:189], v[2:7], v[122:125], v161, v130 op_sel_hi:[0,0,0] cbsz:4 blgp:2
	v_mfma_scale_f32_16x16x128_f8f6f4 v[114:117], v[190:193], v[2:7], v[114:117], v161, v130 op_sel_hi:[0,0,0] cbsz:4 blgp:2
	v_mfma_scale_f32_16x16x128_f8f6f4 v[102:105], v[194:197], v[2:7], v[102:105], v161, v130 op_sel_hi:[0,0,0] cbsz:4 blgp:2
	v_mfma_scale_f32_16x16x128_f8f6f4 v[86:89], v[198:201], v[2:7], v[86:89], v161, v130 op_sel_hi:[0,0,0] cbsz:4 blgp:2
	v_mfma_scale_f32_16x16x128_f8f6f4 v[70:73], v[202:205], v[2:7], v[70:73], v161, v130 op_sel_hi:[0,0,0] cbsz:4 blgp:2
	v_mfma_scale_f32_16x16x128_f8f6f4 v[54:57], v[206:209], v[2:7], v[54:57], v161, v130 op_sel_hi:[0,0,0] cbsz:4 blgp:2
	v_mfma_scale_f32_16x16x128_f8f6f4 v[38:41], v[210:213], v[2:7], v[38:41], v161, v130 op_sel_hi:[0,0,0] cbsz:4 blgp:2
	v_mfma_scale_f32_16x16x128_f8f6f4 v[118:121], v[154:157], v[8:13], v[118:121], v161, v131 op_sel_hi:[0,0,0] cbsz:4 blgp:2
	v_mfma_scale_f32_16x16x128_f8f6f4 v[110:113], v[186:189], v[8:13], v[110:113], v161, v131 op_sel_hi:[0,0,0] cbsz:4 blgp:2
	v_mfma_scale_f32_16x16x128_f8f6f4 v[98:101], v[190:193], v[8:13], v[98:101], v161, v131 op_sel_hi:[0,0,0] cbsz:4 blgp:2
	v_mfma_scale_f32_16x16x128_f8f6f4 v[82:85], v[194:197], v[8:13], v[82:85], v161, v131 op_sel_hi:[0,0,0] cbsz:4 blgp:2
	v_mfma_scale_f32_16x16x128_f8f6f4 v[66:69], v[198:201], v[8:13], v[66:69], v161, v131 op_sel_hi:[0,0,0] cbsz:4 blgp:2
	v_mfma_scale_f32_16x16x128_f8f6f4 v[50:53], v[202:205], v[8:13], v[50:53], v161, v131 op_sel_hi:[0,0,0] cbsz:4 blgp:2
	v_mfma_scale_f32_16x16x128_f8f6f4 v[34:37], v[206:209], v[8:13], v[34:37], v161, v131 op_sel_hi:[0,0,0] cbsz:4 blgp:2
	v_mfma_scale_f32_16x16x128_f8f6f4 v[130:133], v[210:213], v[8:13], v[138:141], v161, v131 op_sel_hi:[0,0,0] cbsz:4 blgp:2
	v_mfma_scale_f32_16x16x128_f8f6f4 v[106:109], v[154:157], v[14:19], v[106:109], v161, v167 op_sel_hi:[0,0,0] cbsz:4 blgp:2
	v_mfma_scale_f32_16x16x128_f8f6f4 v[94:97], v[186:189], v[14:19], v[94:97], v161, v167 op_sel_hi:[0,0,0] cbsz:4 blgp:2
	v_mfma_scale_f32_16x16x128_f8f6f4 v[78:81], v[190:193], v[14:19], v[78:81], v161, v167 op_sel_hi:[0,0,0] cbsz:4 blgp:2
	v_mfma_scale_f32_16x16x128_f8f6f4 v[62:65], v[194:197], v[14:19], v[62:65], v161, v167 op_sel_hi:[0,0,0] cbsz:4 blgp:2
	v_mfma_scale_f32_16x16x128_f8f6f4 v[46:49], v[198:201], v[14:19], v[46:49], v161, v167 op_sel_hi:[0,0,0] cbsz:4 blgp:2
	v_mfma_scale_f32_16x16x128_f8f6f4 v[134:137], v[206:209], v[14:19], v[142:145], v161, v167 op_sel_hi:[0,0,0] cbsz:4 blgp:2
	v_mfma_scale_f32_16x16x128_f8f6f4 v[138:141], v[210:213], v[14:19], v[146:149], v161, v167 op_sel_hi:[0,0,0] cbsz:4 blgp:2
	v_mfma_scale_f32_16x16x128_f8f6f4 v[90:93], v[154:157], v[20:25], v[90:93], v161, v168 op_sel_hi:[0,0,0] cbsz:4 blgp:2
	v_mfma_scale_f32_16x16x128_f8f6f4 v[58:61], v[190:193], v[20:25], v[58:61], v161, v168 op_sel_hi:[0,0,0] cbsz:4 blgp:2
	v_mfma_scale_f32_16x16x128_f8f6f4 v[142:145], v[202:205], v[20:25], v[150:153], v161, v168 op_sel_hi:[0,0,0] cbsz:4 blgp:2
	v_mfma_scale_f32_16x16x128_f8f6f4 v[146:149], v[206:209], v[20:25], v[172:175], v161, v168 op_sel_hi:[0,0,0] cbsz:4 blgp:2
	v_mfma_scale_f32_16x16x128_f8f6f4 v[150:153], v[210:213], v[20:25], v[176:179], v161, v168 op_sel_hi:[0,0,0] cbsz:4 blgp:2
	v_mfma_scale_f32_16x16x128_f8f6f4 v[30:33], v[202:205], v[14:19], v[30:33], v161, v167 op_sel_hi:[0,0,0] cbsz:4 blgp:2
	v_mfma_scale_f32_16x16x128_f8f6f4 v[236:239], v[186:189], v[20:25], v[74:77], v161, v168 op_sel_hi:[0,0,0] cbsz:4 blgp:2
	v_mfma_scale_f32_16x16x128_f8f6f4 v[42:45], v[194:197], v[20:25], v[42:45], v161, v168 op_sel_hi:[0,0,0] cbsz:4 blgp:2
	v_mfma_scale_f32_16x16x128_f8f6f4 v[26:29], v[198:201], v[20:25], v[26:29], v161, v168 op_sel_hi:[0,0,0] cbsz:4 blgp:2
	s_barrier
	ds_read_b128 v[168:171], v166
	ds_read_b128 v[172:175], v166 offset:256
	ds_read_b128 v[176:179], v166 offset:512
	ds_read_b128 v[180:183], v166 offset:768
	ds_read_b128 v[184:187], v166 offset:1024
	ds_read_b128 v[188:191], v166 offset:1280
	ds_read_b128 v[192:195], v166 offset:1536
	ds_read_b128 v[196:199], v166 offset:1792
	ds_read_b64 v[2:3], v162
	ds_read_b64 v[4:5], v162 offset:8
	ds_read_b64 v[6:7], v162 offset:16
	ds_read_b64 v[8:9], v165
	ds_read_b64 v[10:11], v165 offset:8
	ds_read_b64 v[12:13], v165 offset:16
	ds_read_b64 v[14:15], v164
	ds_read_b64 v[16:17], v164 offset:8
	ds_read_b64 v[18:19], v164 offset:16
	ds_read_b64 v[20:21], v163
	ds_read_b64 v[22:23], v163 offset:8
	ds_read_b64 v[24:25], v163 offset:16
	v_add_u32_e32 v154, 0x21800, v248
	v_add_u32_e32 v155, 0x21820, v248
	v_add_u32_e32 v156, 0x21840, v248
	v_add_u32_e32 v157, 0x21860, v248
	ds_read_u16 v166, v154
	ds_read_u16 v167, v155
	ds_read_u16 v74, v156
	ds_read_u16 v75, v157
	s_waitcnt vmcnt(0)
	s_waitcnt lgkmcnt(0)
	s_waitcnt lgkmcnt(0)
	v_mov_b32_e32 v76, v166
	v_mov_b32_e32 v77, v167
	v_mov_b32_e32 v228, v74
	v_mov_b32_e32 v252, v75
	s_barrier
	v_mfma_scale_f32_16x16x128_f8f6f4 v[126:129], v[168:171], v[2:7], v[126:129], v161, v76 op_sel_hi:[0,0,0] cbsz:4 blgp:2
	v_mfma_scale_f32_16x16x128_f8f6f4 v[122:125], v[172:175], v[2:7], v[122:125], v161, v76 op_sel_hi:[0,0,0] cbsz:4 blgp:2
	v_mfma_scale_f32_16x16x128_f8f6f4 v[114:117], v[176:179], v[2:7], v[114:117], v161, v76 op_sel_hi:[0,0,0] cbsz:4 blgp:2
	v_mfma_scale_f32_16x16x128_f8f6f4 v[102:105], v[180:183], v[2:7], v[102:105], v161, v76 op_sel_hi:[0,0,0] cbsz:4 blgp:2
	v_mfma_scale_f32_16x16x128_f8f6f4 v[86:89], v[184:187], v[2:7], v[86:89], v161, v76 op_sel_hi:[0,0,0] cbsz:4 blgp:2
	v_mfma_scale_f32_16x16x128_f8f6f4 v[70:73], v[188:191], v[2:7], v[70:73], v161, v76 op_sel_hi:[0,0,0] cbsz:4 blgp:2
	v_mfma_scale_f32_16x16x128_f8f6f4 v[54:57], v[192:195], v[2:7], v[54:57], v161, v76 op_sel_hi:[0,0,0] cbsz:4 blgp:2
	v_mfma_scale_f32_16x16x128_f8f6f4 v[154:157], v[196:199], v[2:7], v[38:41], v161, v76 op_sel_hi:[0,0,0] cbsz:4 blgp:2
	v_mfma_scale_f32_16x16x128_f8f6f4 v[118:121], v[168:171], v[8:13], v[118:121], v161, v77 op_sel_hi:[0,0,0] cbsz:4 blgp:2
	v_mfma_scale_f32_16x16x128_f8f6f4 v[82:85], v[180:183], v[8:13], v[82:85], v161, v77 op_sel_hi:[0,0,0] cbsz:4 blgp:2
	v_mfma_scale_f32_16x16x128_f8f6f4 v[66:69], v[184:187], v[8:13], v[66:69], v161, v77 op_sel_hi:[0,0,0] cbsz:4 blgp:2
	v_mfma_scale_f32_16x16x128_f8f6f4 v[50:53], v[188:191], v[8:13], v[50:53], v161, v77 op_sel_hi:[0,0,0] cbsz:4 blgp:2
	v_mfma_scale_f32_16x16x128_f8f6f4 v[130:133], v[196:199], v[8:13], v[130:133], v161, v77 op_sel_hi:[0,0,0] cbsz:4 blgp:2
	v_mfma_scale_f32_16x16x128_f8f6f4 v[62:65], v[180:183], v[14:19], v[62:65], v161, v228 op_sel_hi:[0,0,0] cbsz:4 blgp:2
	v_mfma_scale_f32_16x16x128_f8f6f4 v[46:49], v[184:187], v[14:19], v[46:49], v161, v228 op_sel_hi:[0,0,0] cbsz:4 blgp:2
	v_mfma_scale_f32_16x16x128_f8f6f4 v[58:61], v[176:179], v[20:25], v[58:61], v161, v252 op_sel_hi:[0,0,0] cbsz:4 blgp:2
	v_mfma_scale_f32_16x16x128_f8f6f4 v[162:165], v[172:175], v[8:13], v[110:113], v161, v77 op_sel_hi:[0,0,0] cbsz:4 blgp:2
	v_mfma_scale_f32_16x16x128_f8f6f4 v[200:203], v[176:179], v[8:13], v[98:101], v161, v77 op_sel_hi:[0,0,0] cbsz:4 blgp:2
	v_mfma_scale_f32_16x16x128_f8f6f4 v[204:207], v[192:195], v[8:13], v[34:37], v161, v77 op_sel_hi:[0,0,0] cbsz:4 blgp:2
	v_mfma_scale_f32_16x16x128_f8f6f4 v[208:211], v[168:171], v[14:19], v[106:109], v161, v228 op_sel_hi:[0,0,0] cbsz:4 blgp:2
	v_mfma_scale_f32_16x16x128_f8f6f4 v[212:215], v[172:175], v[14:19], v[94:97], v161, v228 op_sel_hi:[0,0,0] cbsz:4 blgp:2
	v_mfma_scale_f32_16x16x128_f8f6f4 v[216:219], v[176:179], v[14:19], v[78:81], v161, v228 op_sel_hi:[0,0,0] cbsz:4 blgp:2
	v_mfma_scale_f32_16x16x128_f8f6f4 v[220:223], v[188:191], v[14:19], v[30:33], v161, v228 op_sel_hi:[0,0,0] cbsz:4 blgp:2
	v_mfma_scale_f32_16x16x128_f8f6f4 v[224:227], v[192:195], v[14:19], v[134:137], v161, v228 op_sel_hi:[0,0,0] cbsz:4 blgp:2
	v_mfma_scale_f32_16x16x128_f8f6f4 v[228:231], v[196:199], v[14:19], v[138:141], v161, v228 op_sel_hi:[0,0,0] cbsz:4 blgp:2
	v_mfma_scale_f32_16x16x128_f8f6f4 v[232:235], v[168:171], v[20:25], v[90:93], v161, v252 op_sel_hi:[0,0,0] cbsz:4 blgp:2
	v_mfma_scale_f32_16x16x128_f8f6f4 v[236:239], v[172:175], v[20:25], v[236:239], v161, v252 op_sel_hi:[0,0,0] cbsz:4 blgp:2
	v_mfma_scale_f32_16x16x128_f8f6f4 v[42:45], v[180:183], v[20:25], v[42:45], v161, v252 op_sel_hi:[0,0,0] cbsz:4 blgp:2
	v_mfma_scale_f32_16x16x128_f8f6f4 v[240:243], v[184:187], v[20:25], v[26:29], v161, v252 op_sel_hi:[0,0,0] cbsz:4 blgp:2
	v_mfma_scale_f32_16x16x128_f8f6f4 v[244:247], v[188:191], v[20:25], v[142:145], v161, v252 op_sel_hi:[0,0,0] cbsz:4 blgp:2
	v_mfma_scale_f32_16x16x128_f8f6f4 v[248:251], v[192:195], v[20:25], v[146:149], v161, v252 op_sel_hi:[0,0,0] cbsz:4 blgp:2
	v_mfma_scale_f32_16x16x128_f8f6f4 v[252:255], v[196:199], v[20:25], v[150:153], v161, v252 op_sel_hi:[0,0,0] cbsz:4 blgp:2
	s_barrier
	ds_read_b64 v[18:19], v1
	ds_read_b64 v[20:21], v1 offset:8
	ds_read_b64 v[22:23], v1 offset:16
	ds_read_b64 v[24:25], v160
	ds_read_b64 v[26:27], v160 offset:8
	ds_read_b64 v[28:29], v160 offset:16
	ds_read_b64 v[30:31], v159
	ds_read_b64 v[32:33], v159 offset:8
	ds_read_b64 v[34:35], v159 offset:16
	ds_read_b64 v[36:37], v158
	ds_read_b64 v[38:39], v158 offset:8
	ds_read_b64 v[40:41], v158 offset:16
	s_waitcnt lgkmcnt(0)
	v_lshrrev_b32_e32 v1, 8, v166
	v_lshrrev_b32_e32 v76, 8, v167
	v_lshrrev_b32_e32 v112, 8, v74
	v_lshrrev_b32_e32 v160, 8, v75
	s_barrier
	v_mfma_scale_f32_16x16x128_f8f6f4 v[14:17], v[168:171], v[18:23], v[126:129], v161, v1 op_sel_hi:[0,0,0] cbsz:4 blgp:2
	v_mfma_scale_f32_16x16x128_f8f6f4 v[10:13], v[172:175], v[18:23], v[122:125], v161, v1 op_sel_hi:[0,0,0] cbsz:4 blgp:2
	v_mfma_scale_f32_16x16x128_f8f6f4 v[6:9], v[176:179], v[18:23], v[114:117], v161, v1 op_sel_hi:[0,0,0] cbsz:4 blgp:2
	v_mfma_scale_f32_16x16x128_f8f6f4 v[2:5], v[180:183], v[18:23], v[102:105], v161, v1 op_sel_hi:[0,0,0] cbsz:4 blgp:2
	v_mfma_scale_f32_16x16x128_f8f6f4 v[108:111], v[184:187], v[18:23], v[86:89], v161, v1 op_sel_hi:[0,0,0] cbsz:4 blgp:2
	v_mfma_scale_f32_16x16x128_f8f6f4 v[104:107], v[188:191], v[18:23], v[70:73], v161, v1 op_sel_hi:[0,0,0] cbsz:4 blgp:2
	v_mfma_scale_f32_16x16x128_f8f6f4 v[100:103], v[192:195], v[18:23], v[54:57], v161, v1 op_sel_hi:[0,0,0] cbsz:4 blgp:2
	v_mfma_scale_f32_16x16x128_f8f6f4 v[96:99], v[196:199], v[18:23], v[154:157], v161, v1 op_sel_hi:[0,0,0] cbsz:4 blgp:2
	v_mfma_scale_f32_16x16x128_f8f6f4 v[156:159], v[168:171], v[24:29], v[118:121], v161, v76 op_sel_hi:[0,0,0] cbsz:4 blgp:2
	v_mfma_scale_f32_16x16x128_f8f6f4 v[152:155], v[172:175], v[24:29], v[162:165], v161, v76 op_sel_hi:[0,0,0] cbsz:4 blgp:2
	v_mfma_scale_f32_16x16x128_f8f6f4 v[148:151], v[176:179], v[24:29], v[200:203], v161, v76 op_sel_hi:[0,0,0] cbsz:4 blgp:2
	v_mfma_scale_f32_16x16x128_f8f6f4 v[144:147], v[180:183], v[24:29], v[82:85], v161, v76 op_sel_hi:[0,0,0] cbsz:4 blgp:2
	v_mfma_scale_f32_16x16x128_f8f6f4 v[92:95], v[184:187], v[24:29], v[66:69], v161, v76 op_sel_hi:[0,0,0] cbsz:4 blgp:2
	v_mfma_scale_f32_16x16x128_f8f6f4 v[88:91], v[188:191], v[24:29], v[50:53], v161, v76 op_sel_hi:[0,0,0] cbsz:4 blgp:2
	v_mfma_scale_f32_16x16x128_f8f6f4 v[84:87], v[192:195], v[24:29], v[204:207], v161, v76 op_sel_hi:[0,0,0] cbsz:4 blgp:2
	v_mfma_scale_f32_16x16x128_f8f6f4 v[80:83], v[196:199], v[24:29], v[130:133], v161, v76 op_sel_hi:[0,0,0] cbsz:4 blgp:2
	v_mfma_scale_f32_16x16x128_f8f6f4 v[140:143], v[168:171], v[30:35], v[208:211], v161, v112 op_sel_hi:[0,0,0] cbsz:4 blgp:2
	v_mfma_scale_f32_16x16x128_f8f6f4 v[136:139], v[172:175], v[30:35], v[212:215], v161, v112 op_sel_hi:[0,0,0] cbsz:4 blgp:2
	v_mfma_scale_f32_16x16x128_f8f6f4 v[132:135], v[176:179], v[30:35], v[216:219], v161, v112 op_sel_hi:[0,0,0] cbsz:4 blgp:2
	v_mfma_scale_f32_16x16x128_f8f6f4 v[128:131], v[180:183], v[30:35], v[62:65], v161, v112 op_sel_hi:[0,0,0] cbsz:4 blgp:2
	v_mfma_scale_f32_16x16x128_f8f6f4 v[76:79], v[184:187], v[30:35], v[46:49], v161, v112 op_sel_hi:[0,0,0] cbsz:4 blgp:2
	v_mfma_scale_f32_16x16x128_f8f6f4 v[72:75], v[188:191], v[30:35], v[220:223], v161, v112 op_sel_hi:[0,0,0] cbsz:4 blgp:2
	v_mfma_scale_f32_16x16x128_f8f6f4 v[68:71], v[192:195], v[30:35], v[224:227], v161, v112 op_sel_hi:[0,0,0] cbsz:4 blgp:2
	v_mfma_scale_f32_16x16x128_f8f6f4 v[64:67], v[196:199], v[30:35], v[228:231], v161, v112 op_sel_hi:[0,0,0] cbsz:4 blgp:2
	v_mfma_scale_f32_16x16x128_f8f6f4 v[124:127], v[168:171], v[36:41], v[232:235], v161, v160 op_sel_hi:[0,0,0] cbsz:4 blgp:2
	v_mfma_scale_f32_16x16x128_f8f6f4 v[120:123], v[172:175], v[36:41], v[236:239], v161, v160 op_sel_hi:[0,0,0] cbsz:4 blgp:2
	v_mfma_scale_f32_16x16x128_f8f6f4 v[116:119], v[176:179], v[36:41], v[58:61], v161, v160 op_sel_hi:[0,0,0] cbsz:4 blgp:2
	v_mfma_scale_f32_16x16x128_f8f6f4 v[112:115], v[180:183], v[36:41], v[42:45], v161, v160 op_sel_hi:[0,0,0] cbsz:4 blgp:2
	v_mfma_scale_f32_16x16x128_f8f6f4 v[60:63], v[184:187], v[36:41], v[240:243], v161, v160 op_sel_hi:[0,0,0] cbsz:4 blgp:2
	v_mfma_scale_f32_16x16x128_f8f6f4 v[56:59], v[188:191], v[36:41], v[244:247], v161, v160 op_sel_hi:[0,0,0] cbsz:4 blgp:2
	v_mfma_scale_f32_16x16x128_f8f6f4 v[52:55], v[192:195], v[36:41], v[248:251], v161, v160 op_sel_hi:[0,0,0] cbsz:4 blgp:2
	v_mfma_scale_f32_16x16x128_f8f6f4 v[48:51], v[196:199], v[36:41], v[252:255], v161, v160 op_sel_hi:[0,0,0] cbsz:4 blgp:2
	s_barrier
	s_cmpk_gt_u32 s33, 0xff
	s_cbranch_scc1 .LBB3_6
	s_barrier
